# MLA loop unrolled over the 3-buffer LDS ring as well (ring bases as immediate offsets, K-fragment addresses loop invariant)
# speedup vs baseline: 1.0077x; 1.0077x over previous
; #define SLOAD(i, j) do { const int _row = KROW(j); skn[i] = *(const bf16x8*)(Knp + (size_t)(_row + sr) * ldk + c8 * 8); sv[i] = *(const bf16x8*)(Vp + (size_t)(_row + sr) * ldv + c8 * 8); \
;         if (krw) skr[i] = *(const bf16x8*)(Krp + (size_t)(_row + sr2) * 32 + c4 * 8); } while (0)
; #define SWRITE(b, i) do { *(LAS bf16x8*)(lds + (b) * BUF + kn_st) = skn[i]; *(LAS bf16x8*)(lds + (b) * BUF + v_stw) = sv[i]; if (krw) *(LAS bf16x8*)(lds + (b) * BUF + kr_st) = skr[i]; } while (0)
; #define SWRITEO(boff, i) do { *(LAS bf16x8*)(lds + (boff) + kn_st) = skn[i]; *(LAS bf16x8*)(lds + (boff) + v_stw) = sv[i]; if (krw) *(LAS bf16x8*)(lds + (boff) + kr_st) = skr[i]; } while (0)
; #define SWAIT() asm volatile("s_waitcnt vmcnt(2)" ::: "memory")
; __device__ __forceinline__ float psm_max(const f32x16& p0, const f32x16& p1) {
;     float pmax = p0[0];
; #pragma unroll
;     for (int r = 1; r < 16; ++r) pmax = fmaxf(pmax, p0[r]);
; #pragma unroll
;     for (int r = 0; r < 16; ++r) pmax = fmaxf(pmax, p1[r]);
;     { auto rr = __builtin_amdgcn_permlane32_swap(__float_as_uint(pmax), __float_as_uint(pmax), false, false);
;       pmax = fmaxf(__uint_as_float(rr[0]), __uint_as_float(rr[1])); }
;     return pmax;
; }
; template <bool FIRST> __device__ __forceinline__ void psm_apply(f32x16& p0, f32x16& p1, float pmax, float& m_reg, f32x16& negm, float& alpha) {
;     alpha = 1.f;
;     if (FIRST || !__builtin_expect(__all(pmax <= THR2), 1)) {
;         const float delta = FIRST ? pmax : fmaxf(pmax, 0.f);
;         if (!FIRST) alpha = __builtin_amdgcn_exp2f(-delta);
;         m_reg += delta;
; #pragma unroll
;         for (int r = 0; r < 16; ++r) { p0[r] -= delta; p1[r] -= delta; negm[r] = -m_reg; }
;     }
; #pragma unroll
;     for (int r = 0; r < 16; ++r) p0[r] = EXP_PROBE ? fmaf(p0[r], 0.001f, 1.f) : __builtin_amdgcn_exp2f(p0[r]);
; }
; template <int DQK, bool FIXM> ...
;     ...
;     __syncthreads();
;     SLOAD(0, 0); asm volatile("s_waitcnt vmcnt(0)" ::: "memory"); SWRITE(0, 0);
;     SLOAD(1, 1); if (2 < NT) SLOAD(0, 2);
;     __syncthreads();
;     qkt<DQK>(pA0, pA1, lds, qr, r32, hi, negm);
;     if (FIXM) { alA = 1.f; _Pragma("unroll") for (int r = 0; r < 16; ++r) pA0[r] = __builtin_amdgcn_exp2f(pA0[r]); } else partialSM<true>(pA0, pA1, m_reg, negm, alA);
;     SWAIT(); SWRITEO(BUF, 1);
.LBB0_520:
	s_or_b64 exec, exec, s[0:1]
	v_add_u32_e32 v15, v208, v209
	s_waitcnt lgkmcnt(0)
	s_barrier
	ds_read_b128 v[34:37], v15
	ds_read_b128 v[38:41], v15 offset:4096
	s_waitcnt lgkmcnt(1)
	v_mfma_f32_32x32x16_bf16 v[50:65], v[34:37], v[166:169], 0
	v_add_u32_e32 v15, v208, v210
	ds_read_b128 v[66:69], v15
	ds_read_b128 v[70:73], v15 offset:4096
	v_add_u32_e32 v15, v208, v211
	s_waitcnt lgkmcnt(2)
	v_mfma_f32_32x32x16_bf16 v[34:49], v[38:41], v[166:169], 0
	s_waitcnt lgkmcnt(1)
	v_mfma_f32_32x32x16_bf16 v[50:65], v[66:69], v[162:165], v[50:65]
	s_waitcnt lgkmcnt(0)
	v_mfma_f32_32x32x16_bf16 v[34:49], v[70:73], v[162:165], v[34:49]
	ds_read_b128 v[66:69], v15
	ds_read_b128 v[70:73], v15 offset:4096
	v_add_u32_e32 v15, v208, v212
	s_waitcnt lgkmcnt(1)
	v_mfma_f32_32x32x16_bf16 v[50:65], v[66:69], v[158:161], v[50:65]
	s_waitcnt lgkmcnt(0)
	v_mfma_f32_32x32x16_bf16 v[34:49], v[70:73], v[158:161], v[34:49]
	ds_read_b128 v[66:69], v15
	ds_read_b128 v[70:73], v15 offset:4096
	v_add_u32_e32 v15, v218, v219
	s_waitcnt lgkmcnt(1)
	v_mfma_f32_32x32x16_bf16 v[50:65], v[66:69], v[154:157], v[50:65]
	s_waitcnt lgkmcnt(0)
	v_mfma_f32_32x32x16_bf16 v[34:49], v[70:73], v[154:157], v[34:49]
	ds_read_b128 v[66:69], v15 offset:8192
	ds_read_b128 v[70:73], v15 offset:10240
	v_add_u32_e32 v15, v218, v220
	s_waitcnt lgkmcnt(1)
	v_mfma_f32_32x32x16_bf16 v[50:65], v[66:69], v[150:153], v[50:65]
	ds_read_b128 v[66:69], v15 offset:8192
	ds_read_b128 v[74:77], v15 offset:10240
	s_waitcnt vmcnt(2)
	s_waitcnt vmcnt(3)
	ds_write_b128 v13, v[4:7] offset:20480
	s_waitcnt vmcnt(2)
	ds_write_b128 v14, v[8:11] offset:32768
	s_waitcnt lgkmcnt(3)
	v_mfma_f32_32x32x16_bf16 v[50:65], v[66:69], v[146:149], v[50:65]
	v_mfma_f32_32x32x16_bf16 v[34:49], v[70:73], v[150:153], v[34:49]
	s_nop 10
	v_max_f32_e32 v15, v51, v51
	v_max_f32_e32 v16, v50, v50
	v_max_f32_e32 v15, v16, v15
	v_max3_f32 v15, v15, v52, v53
	v_max3_f32 v15, v15, v54, v55
	v_max3_f32 v15, v15, v56, v57
	v_max3_f32 v15, v15, v58, v59
	s_waitcnt lgkmcnt(2)
	v_mfma_f32_32x32x16_bf16 v[34:49], v[74:77], v[146:149], v[34:49]
	v_max3_f32 v15, v15, v60, v61
	v_max3_f32 v15, v15, v62, v63
	v_max3_f32 v15, v15, v64, v65
	s_nop 8
	v_max3_f32 v15, v15, v34, v35
	v_max3_f32 v15, v15, v36, v37
	v_max3_f32 v15, v15, v38, v39
	v_max3_f32 v15, v15, v40, v41
	v_max3_f32 v15, v15, v42, v43
	v_max3_f32 v15, v15, v44, v45
	v_max3_f32 v15, v15, v46, v47
	v_max3_f32 v15, v15, v48, v49
	v_mov_b32_e32 v16, v15
	s_nop 1
	v_permlane32_swap_b32_e32 v15, v16
	s_and_saveexec_b64 s[0:1], s[2:3]
	ds_write_b128 v12, v[174:177] offset:28672
	s_or_b64 exec, exec, s[0:1]
	v_max_f32_e32 v4, v16, v16
	v_max_f32_e32 v5, v15, v15
	v_max_f32_e32 v4, v5, v4
	v_sub_f32_e32 v5, v50, v4
	v_sub_f32_e32 v6, v51, v4
	v_sub_f32_e32 v7, v52, v4
	v_sub_f32_e32 v8, v53, v4
	v_sub_f32_e32 v9, v54, v4
	v_sub_f32_e32 v10, v55, v4
	v_sub_f32_e32 v11, v56, v4
	v_sub_f32_e32 v12, v57, v4
	v_sub_f32_e32 v13, v58, v4
	v_sub_f32_e32 v14, v59, v4
	v_sub_f32_e32 v15, v60, v4
	v_sub_f32_e32 v16, v61, v4
	v_sub_f32_e32 v17, v62, v4
	v_sub_f32_e32 v50, v63, v4
	v_sub_f32_e32 v51, v64, v4
	v_sub_f32_e32 v52, v65, v4
	v_exp_f32_e32 v243, v5
	v_exp_f32_e32 v245, v6
	v_exp_f32_e32 v241, v7
	v_exp_f32_e32 v244, v8
	v_exp_f32_e32 v239, v9
	v_exp_f32_e32 v242, v10
	v_exp_f32_e32 v238, v11
	v_exp_f32_e32 v240, v12
	v_exp_f32_e32 v236, v13
	v_exp_f32_e32 v237, v14
	v_exp_f32_e32 v233, v15
	v_exp_f32_e32 v235, v16
	v_exp_f32_e32 v231, v17
	v_exp_f32_e32 v234, v50
	v_exp_f32_e32 v230, v51
	v_exp_f32_e32 v232, v52
	v_add_f32_e32 v224, 0, v4
	v_mov_b32_e32 v16, v3
	v_mov_b32_e32 v17, v3
	v_xor_b32_e32 v82, 0x80000000, v224
	v_sub_f32_e32 v113, v49, v4
	v_sub_f32_e32 v112, v48, v4
	v_sub_f32_e32 v111, v47, v4
	v_sub_f32_e32 v110, v46, v4
	v_sub_f32_e32 v109, v45, v4
	v_sub_f32_e32 v108, v44, v4
	v_sub_f32_e32 v107, v43, v4
	v_sub_f32_e32 v106, v42, v4
	v_sub_f32_e32 v105, v41, v4
	v_sub_f32_e32 v104, v40, v4
	v_sub_f32_e32 v103, v39, v4
	v_sub_f32_e32 v102, v38, v4
	v_sub_f32_e32 v101, v37, v4
	v_sub_f32_e32 v100, v36, v4
	v_sub_f32_e32 v99, v35, v4
	v_sub_f32_e32 v98, v34, v4
	v_lshl_add_u64 v[206:207], s[10:11], 0, v[2:3]
	s_mov_b64 s[42:43], s[10:11]
	v_mov_b32_e32 v2, v3
	v_mov_b32_e32 v4, v3
	v_mov_b32_e32 v5, v3
	v_mov_b32_e32 v6, v3
	v_mov_b32_e32 v7, v3
	v_mov_b32_e32 v8, v3
	v_mov_b32_e32 v9, v3
	v_mov_b32_e32 v10, v3
	v_mov_b32_e32 v11, v3
	v_mov_b32_e32 v12, v3
	v_mov_b32_e32 v13, v3
	v_mov_b32_e32 v14, v3
	v_mov_b32_e32 v15, v3
	v_mov_b64_e32 v[48:49], v[16:17]
	v_mov_b64_e32 v[64:65], v[16:17]
	s_ashr_i32 s9, s8, 31
	s_add_i32 s12, s31, -1
	s_mov_b32 s11, 0
	v_mov_b32_e32 v223, 0
	v_mov_b32_e32 v227, 1.0
	s_movk_i32 s13, 0x5000
	s_mov_b32 s0, 0xa000
	s_mov_b32 s35, 4
	v_readlane_b32 s44, v254, 8
	v_readlane_b32 s45, v254, 9
	s_nop 3
	s_add_u32 s44, s44, 0x1ea00000
	s_addc_u32 s45, s45, 0
	v_subrev_u32_e32 v225, s42, v206
	v_lshlrev_b32_e32 v226, 11, v221
	v_add_u32_e32 v225, v225, v226
	v_add_u32_e32 v225, 0xfff80000, v225
	v_subrev_u32_e32 v226, s44, v204
	v_lshl_add_u32 v226, v215, 6, v226
	v_mov_b64_e32 v[46:47], v[14:15]
	v_mov_b64_e32 v[44:45], v[12:13]
	v_mov_b64_e32 v[42:43], v[10:11]
	v_mov_b64_e32 v[40:41], v[8:9]
	v_mov_b64_e32 v[38:39], v[6:7]
	v_mov_b64_e32 v[36:37], v[4:5]
	v_mov_b64_e32 v[34:35], v[2:3]
	v_mov_b64_e32 v[62:63], v[14:15]
	v_mov_b64_e32 v[60:61], v[12:13]
	v_mov_b64_e32 v[58:59], v[10:11]
	v_mov_b64_e32 v[56:57], v[8:9]
	v_mov_b64_e32 v[54:55], v[6:7]
	v_mov_b64_e32 v[52:53], v[4:5]
	v_mov_b64_e32 v[50:51], v[2:3]
	v_mov_b32_e32 v83, v82
	v_mov_b32_e32 v84, v82
	v_mov_b32_e32 v85, v82
	v_mov_b32_e32 v86, v82
	v_mov_b32_e32 v87, v82
	v_mov_b32_e32 v88, v82
	v_mov_b32_e32 v89, v82
	v_mov_b32_e32 v90, v82
	v_mov_b32_e32 v91, v82
	v_mov_b32_e32 v92, v82
	v_mov_b32_e32 v93, v82
	v_mov_b32_e32 v94, v82
	v_mov_b32_e32 v95, v82
	v_mov_b32_e32 v96, v82
	v_mov_b32_e32 v97, v82
	v_add_u32_e32 v209, v201, v209
	v_add_u32_e32 v210, v201, v210
	v_add_u32_e32 v211, v201, v211
	v_add_u32_e32 v212, v201, v212
	v_add_u32_e32 v219, v217, v219
	v_add_u32_e32 v220, v217, v220
; #define SBAR() __builtin_amdgcn_sched_barrier(0)
; #define ATT_PKN(P, BASE, OUT) do { u32x4 w = {cvt_pk_bf16(P[BASE + 0], P[BASE + 1]), cvt_pk_bf16(P[BASE + 2], P[BASE + 3]), cvt_pk_bf16(P[BASE + 4], P[BASE + 5]), cvt_pk_bf16(P[BASE + 6], P[BASE + 7])}; \
;     OUT = __builtin_bit_cast(bf16x8, w); } while (0)
; #define SLOAD(i, j) do { const int _row = KROW(j); skn[i] = *(const bf16x8*)(Knp + (size_t)(_row + sr) * ldk + c8 * 8); sv[i] = *(const bf16x8*)(Vp + (size_t)(_row + sr) * ldv + c8 * 8); \
;         if (krw) skr[i] = *(const bf16x8*)(Krp + (size_t)(_row + sr2) * 32 + c4 * 8); } while (0)
; #define SWRITEO(boff, i) do { *(LAS bf16x8*)(lds + (boff) + kn_st) = skn[i]; *(LAS bf16x8*)(lds + (boff) + v_stw) = sv[i]; if (krw) *(LAS bf16x8*)(lds + (boff) + kr_st) = skr[i]; } while (0)
; #define PVO(boff) do { pv_one<0>(o0, vb0 + (boff), pa0, pa1, pa2, pa3); pv_one<1>(o1, vb0 + (boff), pa0, pa1, pa2, pa3); } while (0)
; #define SWAIT() asm volatile("s_waitcnt vmcnt(2)" ::: "memory")
; #define ROT() do { const int _t = bV; bV = bK; bK = bW; bW = _t; } while (0)
; __device__ __forceinline__ void finishSM(f32x16& p0, f32x16& p1, float alpha, float& l_reg, bf16x8& pa0, bf16x8& pa1, bf16x8& pa2, bf16x8& pa3) {
; #pragma unroll
;     for (int r = 0; r < 16; ++r) p1[r] = EXP_PROBE ? fmaf(p1[r], 0.001f, 1.f) : __builtin_amdgcn_exp2f(p1[r]);
;     float ps = 0.f;
; #pragma unroll
;     for (int r = 0; r < 16; ++r) ps += p0[r];
; #pragma unroll
;     for (int r = 0; r < 16; ++r) ps += p1[r];
;     { auto rr = __builtin_amdgcn_permlane32_swap(__float_as_uint(ps), __float_as_uint(ps), false, false);
;       ps = __uint_as_float(rr[0]) + __uint_as_float(rr[1]); }
;     l_reg = l_reg * alpha + ps;
;     ATT_PKN(p0, 0, pa0); ATT_PKN(p0, 8, pa1); ATT_PKN(p1, 0, pa2); ATT_PKN(p1, 8, pa3);
; }
; template <int DQK, bool FIXM> ...
;     ...
;     for (int j = 1; j + 1 < NT; j += 2) {
;         if (!NOBAR_PROBE) __syncthreads();
;         SBAR(); qkt<DQK>(pB0, pB1, lds + bK, qr, r32, hi, negm);
;         finishSM(pA0, pA1, alA, l_reg, pa0, pa1, pa2, pa3); SBAR();
;         SLOAD(1, j + 2); SBAR();
;         if constexpr (FIXM) pv_psm<true>(o0, o1, vb0 + bV, pa0, pa1, pa2, pa3, pB0, pB1, m_reg, negm, alB); else { PVO(bV); partialSM<false>(pB0, pB1, m_reg, negm, alB); }
;         SWAIT(); SWRITEO(bW, 0);
;         if (!FIXM) RESC(alB); ROT();
.LBB0_523:
	s_waitcnt lgkmcnt(0)
	s_barrier
	ds_read_b128 v[4:7], v209 offset:20480
	ds_read_b128 v[8:11], v209 offset:24576
	ds_read_b128 v[174:177], v210 offset:20480
	ds_read_b128 v[246:249], v210 offset:24576
	ds_read_b128 v[250:253], v211 offset:20480
	ds_read_b128 v[78:81], v211 offset:24576
	ds_read_b128 v[12:15], v212 offset:20480
	v_exp_f32_e32 v98, v98
	v_exp_f32_e32 v99, v99
	v_exp_f32_e32 v100, v100
	v_exp_f32_e32 v101, v101
	v_exp_f32_e32 v102, v102
	v_exp_f32_e32 v103, v103
	v_exp_f32_e32 v104, v104
	v_exp_f32_e32 v105, v105
	s_waitcnt lgkmcnt(6)
	v_mfma_f32_32x32x16_bf16 v[130:145], v[4:7], v[166:169], v[82:97]
	ds_read_b128 v[4:7], v212 offset:24576
	v_exp_f32_e32 v106, v106
	v_exp_f32_e32 v107, v107
	v_exp_f32_e32 v108, v108
	v_cvt_pk_bf16_f32 v74, v243, v245
	s_waitcnt lgkmcnt(6)
	v_mfma_f32_32x32x16_bf16 v[114:129], v[8:11], v[166:169], v[82:97]
	ds_read_b128 v[8:11], v219 offset:28672
	v_exp_f32_e32 v109, v109
	v_exp_f32_e32 v110, v110
	v_exp_f32_e32 v111, v111
	v_cvt_pk_bf16_f32 v75, v241, v244
	s_waitcnt lgkmcnt(6)
	v_mfma_f32_32x32x16_bf16 v[130:145], v[174:177], v[162:165], v[130:145]
	ds_read_b128 v[174:177], v219 offset:30720
	v_exp_f32_e32 v112, v112
	v_exp_f32_e32 v113, v113
	v_cvt_pk_bf16_f32 v76, v239, v242
	v_cvt_pk_bf16_f32 v77, v238, v240
	v_add_f32_e32 v229, 0, v243
	v_add_f32_e32 v229, v245, v229
	s_waitcnt lgkmcnt(6)
	v_mfma_f32_32x32x16_bf16 v[114:129], v[246:249], v[162:165], v[114:129]
	ds_read_b128 v[246:249], v220 offset:28672
	v_cvt_pk_bf16_f32 v66, v236, v237
	v_cvt_pk_bf16_f32 v67, v233, v235
	v_add_f32_e32 v229, v241, v229
	v_add_f32_e32 v229, v244, v229
	v_add_f32_e32 v229, v239, v229
	v_add_f32_e32 v229, v242, v229
	s_waitcnt lgkmcnt(6)
	v_mfma_f32_32x32x16_bf16 v[130:145], v[250:253], v[158:161], v[130:145]
	ds_read_b128 v[250:253], v220 offset:30720
	v_cvt_pk_bf16_f32 v68, v231, v234
	v_cvt_pk_bf16_f32 v69, v230, v232
	v_add_f32_e32 v229, v238, v229
	v_add_f32_e32 v229, v240, v229
	v_add_f32_e32 v229, v236, v229
	v_add_f32_e32 v229, v237, v229
	s_waitcnt lgkmcnt(6)
	v_mfma_f32_32x32x16_bf16 v[114:129], v[78:81], v[158:161], v[114:129]
	v_add_f32_e32 v229, v233, v229
	v_add_f32_e32 v229, v235, v229
	v_add_f32_e32 v229, v231, v229
	v_add_f32_e32 v229, v234, v229
	v_add_f32_e32 v229, v230, v229
	v_add_f32_e32 v229, v232, v229
	s_waitcnt lgkmcnt(5)
	v_mfma_f32_32x32x16_bf16 v[130:145], v[12:15], v[154:157], v[130:145]
	ds_read_b64_tr_b16 v[230:231], v213 offset:0
	ds_read_b64_tr_b16 v[232:233], v213 offset:1024
	ds_read_b64_tr_b16 v[234:235], v213 offset:2048
	ds_read_b64_tr_b16 v[236:237], v213 offset:3072
	v_add_f32_e32 v229, v98, v229
	v_add_f32_e32 v229, v99, v229
	v_add_f32_e32 v229, v100, v229
	s_waitcnt lgkmcnt(8)
	v_mfma_f32_32x32x16_bf16 v[114:129], v[4:7], v[154:157], v[114:129]
	ds_read_b64_tr_b16 v[238:239], v213 offset:4096
	ds_read_b64_tr_b16 v[240:241], v213 offset:5120
	ds_read_b64_tr_b16 v[242:243], v213 offset:6144
	ds_read_b64_tr_b16 v[244:245], v213 offset:7168
	v_add_f32_e32 v229, v101, v229
	v_add_f32_e32 v229, v102, v229
	v_add_f32_e32 v229, v103, v229
	s_waitcnt lgkmcnt(11)
	v_mfma_f32_32x32x16_bf16 v[130:145], v[8:11], v[150:153], v[130:145]
	v_add_f32_e32 v229, v104, v229
	v_add_f32_e32 v229, v105, v229
	v_add_f32_e32 v229, v106, v229
	v_add_f32_e32 v229, v107, v229
	v_add_f32_e32 v229, v108, v229
	v_add_f32_e32 v229, v109, v229
	s_waitcnt lgkmcnt(10)
	v_mfma_f32_32x32x16_bf16 v[114:129], v[174:177], v[150:153], v[114:129]
	v_add_f32_e32 v229, v110, v229
	v_add_f32_e32 v229, v111, v229
	v_add_f32_e32 v229, v112, v229
	v_add_f32_e32 v228, v113, v229
	v_mov_b32_e32 v229, v228
	s_add_i32 s36, s35, -1
	s_cmp_lt_u32 s36, s30
	s_cselect_b32 s0, 0, s30
	s_cselect_b32 s1, s29, s34
	s_lshl_b32 s0, s0, 6
	s_sub_i32 s37, s1, s0
	s_lshl_b32 s1, s36, 6
	s_add_i32 s37, s37, s1
	s_lshl_b32 s0, s37, 6
	s_add_u32 s48, s44, s0
	s_addc_u32 s49, s45, 0
	s_lshl_b32 s0, s37, 11
	s_add_u32 s46, s42, s0
	s_addc_u32 s47, s43, 0
	global_load_dwordx4 v[174:177], v226, s[48:49]
	s_waitcnt lgkmcnt(9)
	v_mfma_f32_32x32x16_bf16 v[130:145], v[246:249], v[146:149], v[130:145]
	v_cvt_pk_bf16_f32 v70, v98, v99
	v_cvt_pk_bf16_f32 v71, v100, v101
	v_cvt_pk_bf16_f32 v72, v102, v103
	v_cvt_pk_bf16_f32 v73, v104, v105
	v_permlane32_swap_b32_e32 v228, v229
	global_load_dwordx4 v[8:11], v225, s[46:47]
	global_load_dwordx4 v[4:7], v225, s[46:47] offset:128
	s_waitcnt lgkmcnt(8)
	v_mfma_f32_32x32x16_bf16 v[114:129], v[250:253], v[146:149], v[114:129]
	v_cvt_pk_bf16_f32 v12, v106, v107
	v_cvt_pk_bf16_f32 v13, v108, v109
	v_cvt_pk_bf16_f32 v14, v110, v111
	v_cvt_pk_bf16_f32 v15, v112, v113
	ds_read_b64_tr_b16 v[78:79], v213 offset:512
	ds_read_b64_tr_b16 v[80:81], v213 offset:1536
	ds_read_b64_tr_b16 v[98:99], v213 offset:2560
	ds_read_b64_tr_b16 v[100:101], v213 offset:3584
	ds_read_b64_tr_b16 v[102:103], v213 offset:4608
	ds_read_b64_tr_b16 v[104:105], v213 offset:5632
	ds_read_b64_tr_b16 v[110:111], v213 offset:6656
	ds_read_b64_tr_b16 v[112:113], v213 offset:7680
	v_max3_f32 v2, v130, v131, v132
	v_max3_f32 v2, v2, v133, v134
	v_max3_f32 v2, v2, v135, v136
	v_max3_f32 v2, v2, v137, v138
	v_max3_f32 v2, v2, v139, v140
	v_max3_f32 v2, v2, v141, v142
	v_max3_f32 v2, v2, v143, v144
	v_max3_f32 v2, v2, v145, v114
	v_max3_f32 v2, v2, v115, v116
	s_waitcnt lgkmcnt(8)
	v_mfma_f32_32x32x16_bf16 v[50:65], v[230:233], v[74:77], v[50:65]
	v_max3_f32 v2, v2, v117, v118
	v_max3_f32 v2, v2, v119, v120
	v_max3_f32 v2, v2, v121, v122
	v_mfma_f32_32x32x16_bf16 v[50:65], v[234:237], v[66:69], v[50:65]
	v_max3_f32 v2, v2, v123, v124
	v_max3_f32 v2, v2, v125, v126
	v_max3_f32 v2, v2, v127, v128
	v_mfma_f32_32x32x16_bf16 v[50:65], v[238:241], v[70:73], v[50:65]
	v_max_f32_e32 v2, v2, v129
	s_nop 0
	s_nop 0
	v_mfma_f32_32x32x16_bf16 v[50:65], v[242:245], v[12:15], v[50:65]
	v_mov_b32_e32 v16, v2
	s_nop 1
	v_permlane32_swap_b32_e32 v2, v16
	v_max_f32_e32 v2, v2, v16
	v_cmp_ge_f32_e32 vcc, s28, v2
	s_cmp_eq_u64 vcc, exec
	s_cbranch_scc0 .LBB0_542_0
	v_mov_b32_e32 v2, 1.0
.LBB0_527_0:
	s_waitcnt lgkmcnt(0)
	v_mfma_f32_32x32x16_bf16 v[34:49], v[78:81], v[74:77], v[34:49]
	s_waitcnt vmcnt(3)
	ds_write_b128 v187, v[178:181] offset:40960
	ds_write_b128 v214, v[182:185] offset:53248
	s_cmp_eq_u64 s[2:3], 0
	s_cbranch_scc1 .Lmla_a_nokr_0
	ds_write_b128 v216, v[170:173] offset:49152

; #define SBAR() __builtin_amdgcn_sched_barrier(0)
; #define SLOAD(i, j) do { const int _row = KROW(j); skn[i] = *(const bf16x8*)(Knp + (size_t)(_row + sr) * ldk + c8 * 8); sv[i] = *(const bf16x8*)(Vp + (size_t)(_row + sr) * ldv + c8 * 8); \
;         if (krw) skr[i] = *(const bf16x8*)(Krp + (size_t)(_row + sr2) * 32 + c4 * 8); } while (0)
; #define SWRITEO(boff, i) do { *(LAS bf16x8*)(lds + (boff) + kn_st) = skn[i]; *(LAS bf16x8*)(lds + (boff) + v_stw) = sv[i]; if (krw) *(LAS bf16x8*)(lds + (boff) + kr_st) = skr[i]; } while (0)
; #define PVO(boff) do { pv_one<0>(o0, vb0 + (boff), pa0, pa1, pa2, pa3); pv_one<1>(o1, vb0 + (boff), pa0, pa1, pa2, pa3); } while (0)
; #define SWAIT() asm volatile("s_waitcnt vmcnt(2)" ::: "memory")
; #define RESC(a) do { if (__any((a) < 1.f)) { _Pragma("unroll") for (int r = 0; r < 16; ++r) { o0[r] *= (a); o1[r] *= (a); } } } while (0)
; #define ROT() do { const int _t = bV; bV = bK; bK = bW; bW = _t; } while (0)
; template <int D0> __device__ __forceinline__ void pv_one(f32x16& od, unsigned vb, bf16x8 pa0, bf16x8 pa1, bf16x8 pa2, bf16x8 pa3) {
;     const s16x4 l0 = tr_read<v_rd_off(D0, 0, 0)>(vb), h0 = tr_read<v_rd_off(D0, 0, 1)>(vb), l1 = tr_read<v_rd_off(D0, 1, 0)>(vb), h1 = tr_read<v_rd_off(D0, 1, 1)>(vb);
;     const s16x4 l2 = tr_read<v_rd_off(D0, 2, 0)>(vb), h2 = tr_read<v_rd_off(D0, 2, 1)>(vb), l3 = tr_read<v_rd_off(D0, 3, 0)>(vb), h3 = tr_read<v_rd_off(D0, 3, 1)>(vb);
;     asm volatile("s_waitcnt lgkmcnt(0)" ::: "memory"); SBAR();
;     ...
;     od = __builtin_amdgcn_mfma_f32_32x32x16_bf16(ATT_PK(l0, h0), pa0, od, 0, 0, 0);
;     od = __builtin_amdgcn_mfma_f32_32x32x16_bf16(ATT_PK(l1, h1), pa1, od, 0, 0, 0);
;     od = __builtin_amdgcn_mfma_f32_32x32x16_bf16(ATT_PK(l2, h2), pa2, od, 0, 0, 0);
;     od = __builtin_amdgcn_mfma_f32_32x32x16_bf16(ATT_PK(l3, h3), pa3, od, 0, 0, 0);
;     ...
; }
; template <int DQK, bool FIXM> ...
;     ...
;         if (!NOBAR_PROBE) __syncthreads();
;         SBAR(); qkt<DQK>(pA0, pA1, lds + bK, qr, r32, hi, negm);
;         finishSM(pB0, pB1, alB, l_reg, pa0, pa1, pa2, pa3); SBAR();
;         if (j + 3 < NT) SLOAD(0, j + 3); SBAR();
;         if constexpr (FIXM) pv_psm<true>(o0, o1, vb0 + bV, pa0, pa1, pa2, pa3, pA0, pA1, m_reg, negm, alA); else { PVO(bV); partialSM<false>(pA0, pA1, m_reg, negm, alA); }
;         SWAIT(); SWRITEO(bW, 1);
;         if (!FIXM) RESC(alA); ROT();
.LBB0_531_0:
	s_waitcnt lgkmcnt(0)
	s_barrier
	ds_read_b128 v[178:181], v209 offset:40960
	ds_read_b128 v[182:185], v209 offset:45056
	ds_read_b128 v[170:173], v210 offset:40960
	ds_read_b128 v[66:69], v210 offset:45056
	ds_read_b128 v[70:73], v211 offset:40960
	ds_read_b128 v[74:77], v211 offset:45056
	ds_read_b128 v[78:81], v212 offset:40960
	v_exp_f32_e32 v114, v114
	v_exp_f32_e32 v115, v115
	v_exp_f32_e32 v116, v116
	v_exp_f32_e32 v117, v117
	v_exp_f32_e32 v118, v118
	v_exp_f32_e32 v119, v119
	v_exp_f32_e32 v120, v120
	v_exp_f32_e32 v121, v121
	s_waitcnt lgkmcnt(6)
	v_mfma_f32_32x32x16_bf16 v[130:145], v[178:181], v[166:169], v[82:97]
	ds_read_b128 v[178:181], v212 offset:45056
	v_exp_f32_e32 v122, v122
	v_exp_f32_e32 v123, v123
	v_exp_f32_e32 v124, v124
	v_cvt_pk_bf16_f32 v12, v16, v234
	s_waitcnt lgkmcnt(6)
	v_mfma_f32_32x32x16_bf16 v[98:113], v[182:185], v[166:169], v[82:97]
	ds_read_b128 v[182:185], v219 offset:49152
	v_exp_f32_e32 v125, v125
	v_exp_f32_e32 v126, v126
	v_exp_f32_e32 v127, v127
	v_cvt_pk_bf16_f32 v13, v235, v236
	s_waitcnt lgkmcnt(6)
	v_mfma_f32_32x32x16_bf16 v[130:145], v[170:173], v[162:165], v[130:145]
	ds_read_b128 v[170:173], v219 offset:51200
	v_exp_f32_e32 v128, v128
	v_exp_f32_e32 v129, v129
	v_cvt_pk_bf16_f32 v14, v237, v238
	v_cvt_pk_bf16_f32 v15, v239, v240
	v_add_f32_e32 v252, 0, v16
	v_add_f32_e32 v252, v234, v252
	s_waitcnt lgkmcnt(6)
	v_mfma_f32_32x32x16_bf16 v[98:113], v[66:69], v[162:165], v[98:113]
	ds_read_b128 v[66:69], v220 offset:49152
	v_cvt_pk_bf16_f32 v230, v241, v242
	v_cvt_pk_bf16_f32 v231, v243, v244
	v_add_f32_e32 v252, v235, v252
	v_add_f32_e32 v252, v236, v252
	v_add_f32_e32 v252, v237, v252
	v_add_f32_e32 v252, v238, v252
	s_waitcnt lgkmcnt(6)
	v_mfma_f32_32x32x16_bf16 v[130:145], v[70:73], v[158:161], v[130:145]
	ds_read_b128 v[70:73], v220 offset:51200
	v_cvt_pk_bf16_f32 v232, v245, v246
	v_cvt_pk_bf16_f32 v233, v247, v248
	v_add_f32_e32 v252, v239, v252
	v_add_f32_e32 v252, v240, v252
	v_add_f32_e32 v252, v241, v252
	v_add_f32_e32 v252, v242, v252
	s_waitcnt lgkmcnt(6)
	v_mfma_f32_32x32x16_bf16 v[98:113], v[74:77], v[158:161], v[98:113]
	v_add_f32_e32 v252, v243, v252
	v_add_f32_e32 v252, v244, v252
	v_add_f32_e32 v252, v245, v252
	v_add_f32_e32 v252, v246, v252
	v_add_f32_e32 v252, v247, v252
	v_add_f32_e32 v252, v248, v252
	s_waitcnt lgkmcnt(5)
	v_mfma_f32_32x32x16_bf16 v[130:145], v[78:81], v[154:157], v[130:145]
	ds_read_b64_tr_b16 v[234:235], v213 offset:20480
	ds_read_b64_tr_b16 v[236:237], v213 offset:21504
	ds_read_b64_tr_b16 v[238:239], v213 offset:22528
	ds_read_b64_tr_b16 v[240:241], v213 offset:23552
	v_add_f32_e32 v252, v114, v252
	v_add_f32_e32 v252, v115, v252
	v_add_f32_e32 v252, v116, v252
	s_waitcnt lgkmcnt(8)
	v_mfma_f32_32x32x16_bf16 v[98:113], v[178:181], v[154:157], v[98:113]
	ds_read_b64_tr_b16 v[242:243], v213 offset:24576
	ds_read_b64_tr_b16 v[244:245], v213 offset:25600
	ds_read_b64_tr_b16 v[246:247], v213 offset:26624
	ds_read_b64_tr_b16 v[248:249], v213 offset:27648
	v_add_f32_e32 v252, v117, v252
	v_add_f32_e32 v252, v118, v252
	v_add_f32_e32 v252, v119, v252
	s_waitcnt lgkmcnt(11)
	v_mfma_f32_32x32x16_bf16 v[130:145], v[182:185], v[150:153], v[130:145]
	v_add_f32_e32 v252, v120, v252
	v_add_f32_e32 v252, v121, v252
	v_add_f32_e32 v252, v122, v252
	v_add_f32_e32 v252, v123, v252
	v_add_f32_e32 v252, v124, v252
	v_add_f32_e32 v252, v125, v252
	s_waitcnt lgkmcnt(10)
	v_mfma_f32_32x32x16_bf16 v[98:113], v[170:173], v[150:153], v[98:113]
	v_add_f32_e32 v252, v126, v252
	v_add_f32_e32 v252, v127, v252
	v_add_f32_e32 v252, v128, v252
	s_waitcnt lgkmcnt(9)
	v_mfma_f32_32x32x16_bf16 v[130:145], v[66:69], v[146:149], v[130:145]
	v_cvt_pk_bf16_f32 v114, v114, v115
	v_cvt_pk_bf16_f32 v115, v116, v117
	v_cvt_pk_bf16_f32 v116, v118, v119
	v_cvt_pk_bf16_f32 v117, v120, v121
	s_cmp_ge_u32 s35, s31
	s_cbranch_scc1 .Lmla_b_noload_0
	s_cmp_lt_u32 s35, s30
	s_cselect_b32 s0, 0, s30
	s_cselect_b32 s1, s29, s34
	s_lshl_b32 s0, s0, 6
	s_sub_i32 s37, s1, s0
	s_lshl_b32 s1, s35, 6
	s_add_i32 s37, s37, s1
	s_lshl_b32 s0, s37, 6
	s_add_u32 s48, s44, s0
	s_addc_u32 s49, s45, 0
	s_lshl_b32 s0, s37, 11
	s_add_u32 s46, s42, s0
	s_addc_u32 s47, s43, 0
	global_load_dwordx4 v[170:173], v226, s[48:49]
	global_load_dwordx4 v[178:181], v225, s[46:47]
	global_load_dwordx4 v[182:185], v225, s[46:47] offset:128
.Lmla_b_ld_done_0:
	s_waitcnt lgkmcnt(8)
	v_mfma_f32_32x32x16_bf16 v[98:113], v[70:73], v[146:149], v[98:113]
	v_cvt_pk_bf16_f32 v118, v122, v123
	v_cvt_pk_bf16_f32 v119, v124, v125
	v_cvt_pk_bf16_f32 v120, v126, v127
	v_cvt_pk_bf16_f32 v121, v128, v129
	v_add_f32_e32 v126, v129, v252
	v_mov_b32_e32 v127, v126
	ds_read_b64_tr_b16 v[66:67], v213 offset:20992
	ds_read_b64_tr_b16 v[68:69], v213 offset:22016
	ds_read_b64_tr_b16 v[70:71], v213 offset:23040
	ds_read_b64_tr_b16 v[72:73], v213 offset:24064
	ds_read_b64_tr_b16 v[74:75], v213 offset:25088
	ds_read_b64_tr_b16 v[76:77], v213 offset:26112
	ds_read_b64_tr_b16 v[78:79], v213 offset:27136
	ds_read_b64_tr_b16 v[80:81], v213 offset:28160
	v_permlane32_swap_b32_e32 v126, v127
	v_max3_f32 v250, v130, v131, v132
	v_max3_f32 v250, v250, v133, v134
	v_max3_f32 v250, v250, v135, v136
	v_max3_f32 v250, v250, v137, v138
	v_max3_f32 v250, v250, v139, v140
	v_max3_f32 v250, v250, v141, v142
	v_max3_f32 v250, v250, v143, v144
	v_max3_f32 v250, v250, v145, v98
	v_max3_f32 v250, v250, v99, v100
	s_waitcnt lgkmcnt(8)
	v_mfma_f32_32x32x16_bf16 v[50:65], v[234:237], v[12:15], v[50:65]
	v_max3_f32 v250, v250, v101, v102
	v_max3_f32 v250, v250, v103, v104
	v_max3_f32 v250, v250, v105, v106
	v_mfma_f32_32x32x16_bf16 v[50:65], v[238:241], v[230:233], v[50:65]
	v_max3_f32 v250, v250, v107, v108
	v_max3_f32 v250, v250, v109, v110
	v_max3_f32 v250, v250, v111, v112
	v_mfma_f32_32x32x16_bf16 v[50:65], v[242:245], v[114:117], v[50:65]
	v_max_f32_e32 v250, v250, v113
	s_nop 0
	s_nop 0
	v_mfma_f32_32x32x16_bf16 v[50:65], v[246:249], v[118:121], v[50:65]
	v_mov_b32_e32 v251, v250
	s_nop 1
	v_permlane32_swap_b32_e32 v250, v251
	v_max_f32_e32 v250, v250, v251
	v_cmp_ge_f32_e32 vcc, s28, v250
	s_cmp_eq_u64 vcc, exec
	v_mov_b32_e32 v16, 1.0
	s_cbranch_scc0 .LBB0_543_0
.LBB0_536_0:
	s_waitcnt lgkmcnt(0)
	v_mfma_f32_32x32x16_bf16 v[34:49], v[66:69], v[12:15], v[34:49]
	s_waitcnt vmcnt(3)
	ds_write_b128 v187, v[8:11] offset:0
	ds_write_b128 v214, v[4:7] offset:12288
	s_cmp_eq_u64 s[2:3], 0
	s_cbranch_scc1 .Lmla_b_nokr_0
	ds_write_b128 v216, v[174:177] offset:8192

; #define SBAR() __builtin_amdgcn_sched_barrier(0)
; #define ATT_PKN(P, BASE, OUT) do { u32x4 w = {cvt_pk_bf16(P[BASE + 0], P[BASE + 1]), cvt_pk_bf16(P[BASE + 2], P[BASE + 3]), cvt_pk_bf16(P[BASE + 4], P[BASE + 5]), cvt_pk_bf16(P[BASE + 6], P[BASE + 7])}; \
;     OUT = __builtin_bit_cast(bf16x8, w); } while (0)
; #define SLOAD(i, j) do { const int _row = KROW(j); skn[i] = *(const bf16x8*)(Knp + (size_t)(_row + sr) * ldk + c8 * 8); sv[i] = *(const bf16x8*)(Vp + (size_t)(_row + sr) * ldv + c8 * 8); \
;         if (krw) skr[i] = *(const bf16x8*)(Krp + (size_t)(_row + sr2) * 32 + c4 * 8); } while (0)
; #define SWRITEO(boff, i) do { *(LAS bf16x8*)(lds + (boff) + kn_st) = skn[i]; *(LAS bf16x8*)(lds + (boff) + v_stw) = sv[i]; if (krw) *(LAS bf16x8*)(lds + (boff) + kr_st) = skr[i]; } while (0)
; #define PVO(boff) do { pv_one<0>(o0, vb0 + (boff), pa0, pa1, pa2, pa3); pv_one<1>(o1, vb0 + (boff), pa0, pa1, pa2, pa3); } while (0)
; #define SWAIT() asm volatile("s_waitcnt vmcnt(2)" ::: "memory")
; #define ROT() do { const int _t = bV; bV = bK; bK = bW; bW = _t; } while (0)
; __device__ __forceinline__ void finishSM(f32x16& p0, f32x16& p1, float alpha, float& l_reg, bf16x8& pa0, bf16x8& pa1, bf16x8& pa2, bf16x8& pa3) {
; #pragma unroll
;     for (int r = 0; r < 16; ++r) p1[r] = EXP_PROBE ? fmaf(p1[r], 0.001f, 1.f) : __builtin_amdgcn_exp2f(p1[r]);
;     float ps = 0.f;
; #pragma unroll
;     for (int r = 0; r < 16; ++r) ps += p0[r];
; #pragma unroll
;     for (int r = 0; r < 16; ++r) ps += p1[r];
;     { auto rr = __builtin_amdgcn_permlane32_swap(__float_as_uint(ps), __float_as_uint(ps), false, false);
;       ps = __uint_as_float(rr[0]) + __uint_as_float(rr[1]); }
;     l_reg = l_reg * alpha + ps;
;     ATT_PKN(p0, 0, pa0); ATT_PKN(p0, 8, pa1); ATT_PKN(p1, 0, pa2); ATT_PKN(p1, 8, pa3);
; }
; template <int DQK, bool FIXM> ...
;     ...
;     for (int j = 1; j + 1 < NT; j += 2) {
;         if (!NOBAR_PROBE) __syncthreads();
;         SBAR(); qkt<DQK>(pB0, pB1, lds + bK, qr, r32, hi, negm);
;         finishSM(pA0, pA1, alA, l_reg, pa0, pa1, pa2, pa3); SBAR();
;         SLOAD(1, j + 2); SBAR();
;         if constexpr (FIXM) pv_psm<true>(o0, o1, vb0 + bV, pa0, pa1, pa2, pa3, pB0, pB1, m_reg, negm, alB); else { PVO(bV); partialSM<false>(pB0, pB1, m_reg, negm, alB); }
;         SWAIT(); SWRITEO(bW, 0);
;         if (!FIXM) RESC(alB); ROT();
.LBB0_540_0:
	v_add_f32_e32 v4, v228, v229
	v_fmac_f32_e32 v4, v227, v223
	v_add_f32_e32 v223, v126, v127
	s_add_i32 s35, s35, 2
	v_fmac_f32_e32 v223, v4, v2
	s_cmp_ge_u32 s36, s12
	s_cbranch_scc1 .Lmla_exit_0
	v_mov_b32_e32 v227, v16
	s_waitcnt lgkmcnt(0)
	s_barrier
	ds_read_b128 v[4:7], v209 offset:0
	ds_read_b128 v[8:11], v209 offset:4096
	ds_read_b128 v[174:177], v210 offset:0
	ds_read_b128 v[246:249], v210 offset:4096
	ds_read_b128 v[250:253], v211 offset:0
	ds_read_b128 v[78:81], v211 offset:4096
	ds_read_b128 v[12:15], v212 offset:0
	v_exp_f32_e32 v98, v98
	v_exp_f32_e32 v99, v99
	v_exp_f32_e32 v100, v100
	v_exp_f32_e32 v101, v101
	v_exp_f32_e32 v102, v102
	v_exp_f32_e32 v103, v103
	v_exp_f32_e32 v104, v104
	v_exp_f32_e32 v105, v105
	s_waitcnt lgkmcnt(6)
	v_mfma_f32_32x32x16_bf16 v[130:145], v[4:7], v[166:169], v[82:97]
	ds_read_b128 v[4:7], v212 offset:4096
	v_exp_f32_e32 v106, v106
	v_exp_f32_e32 v107, v107
	v_exp_f32_e32 v108, v108
	v_cvt_pk_bf16_f32 v74, v243, v245
	s_waitcnt lgkmcnt(6)
	v_mfma_f32_32x32x16_bf16 v[114:129], v[8:11], v[166:169], v[82:97]
	ds_read_b128 v[8:11], v219 offset:8192
	v_exp_f32_e32 v109, v109
	v_exp_f32_e32 v110, v110
	v_exp_f32_e32 v111, v111
	v_cvt_pk_bf16_f32 v75, v241, v244
	s_waitcnt lgkmcnt(6)
	v_mfma_f32_32x32x16_bf16 v[130:145], v[174:177], v[162:165], v[130:145]
	ds_read_b128 v[174:177], v219 offset:10240
	v_exp_f32_e32 v112, v112
	v_exp_f32_e32 v113, v113
	v_cvt_pk_bf16_f32 v76, v239, v242
	v_cvt_pk_bf16_f32 v77, v238, v240
	v_add_f32_e32 v229, 0, v243
	v_add_f32_e32 v229, v245, v229
	s_waitcnt lgkmcnt(6)
	v_mfma_f32_32x32x16_bf16 v[114:129], v[246:249], v[162:165], v[114:129]
	ds_read_b128 v[246:249], v220 offset:8192
	v_cvt_pk_bf16_f32 v66, v236, v237
	v_cvt_pk_bf16_f32 v67, v233, v235
	v_add_f32_e32 v229, v241, v229
	v_add_f32_e32 v229, v244, v229
	v_add_f32_e32 v229, v239, v229
	v_add_f32_e32 v229, v242, v229
	s_waitcnt lgkmcnt(6)
	v_mfma_f32_32x32x16_bf16 v[130:145], v[250:253], v[158:161], v[130:145]
	ds_read_b128 v[250:253], v220 offset:10240
	v_cvt_pk_bf16_f32 v68, v231, v234
	v_cvt_pk_bf16_f32 v69, v230, v232
	v_add_f32_e32 v229, v238, v229
	v_add_f32_e32 v229, v240, v229
	v_add_f32_e32 v229, v236, v229
	v_add_f32_e32 v229, v237, v229
	s_waitcnt lgkmcnt(6)
	v_mfma_f32_32x32x16_bf16 v[114:129], v[78:81], v[158:161], v[114:129]
	v_add_f32_e32 v229, v233, v229
	v_add_f32_e32 v229, v235, v229
	v_add_f32_e32 v229, v231, v229
	v_add_f32_e32 v229, v234, v229
	v_add_f32_e32 v229, v230, v229
	v_add_f32_e32 v229, v232, v229
	s_waitcnt lgkmcnt(5)
	v_mfma_f32_32x32x16_bf16 v[130:145], v[12:15], v[154:157], v[130:145]
	ds_read_b64_tr_b16 v[230:231], v213 offset:40960
	ds_read_b64_tr_b16 v[232:233], v213 offset:41984
	ds_read_b64_tr_b16 v[234:235], v213 offset:43008
	ds_read_b64_tr_b16 v[236:237], v213 offset:44032
	v_add_f32_e32 v229, v98, v229
	v_add_f32_e32 v229, v99, v229
	v_add_f32_e32 v229, v100, v229
	s_waitcnt lgkmcnt(8)
	v_mfma_f32_32x32x16_bf16 v[114:129], v[4:7], v[154:157], v[114:129]
	ds_read_b64_tr_b16 v[238:239], v213 offset:45056
	ds_read_b64_tr_b16 v[240:241], v213 offset:46080
	ds_read_b64_tr_b16 v[242:243], v213 offset:47104
	ds_read_b64_tr_b16 v[244:245], v213 offset:48128
	v_add_f32_e32 v229, v101, v229
	v_add_f32_e32 v229, v102, v229
	v_add_f32_e32 v229, v103, v229
	s_waitcnt lgkmcnt(11)
	v_mfma_f32_32x32x16_bf16 v[130:145], v[8:11], v[150:153], v[130:145]
	v_add_f32_e32 v229, v104, v229
	v_add_f32_e32 v229, v105, v229
	v_add_f32_e32 v229, v106, v229
	v_add_f32_e32 v229, v107, v229
	v_add_f32_e32 v229, v108, v229
	v_add_f32_e32 v229, v109, v229
	s_waitcnt lgkmcnt(10)
	v_mfma_f32_32x32x16_bf16 v[114:129], v[174:177], v[150:153], v[114:129]
	v_add_f32_e32 v229, v110, v229
	v_add_f32_e32 v229, v111, v229
	v_add_f32_e32 v229, v112, v229
	v_add_f32_e32 v228, v113, v229
	v_mov_b32_e32 v229, v228
	s_add_i32 s36, s35, -1
	s_cmp_lt_u32 s36, s30
	s_cselect_b32 s0, 0, s30
	s_cselect_b32 s1, s29, s34
	s_lshl_b32 s0, s0, 6
	s_sub_i32 s37, s1, s0
	s_lshl_b32 s1, s36, 6
	s_add_i32 s37, s37, s1
	s_lshl_b32 s0, s37, 6
	s_add_u32 s48, s44, s0
	s_addc_u32 s49, s45, 0
	s_lshl_b32 s0, s37, 11
	s_add_u32 s46, s42, s0
	s_addc_u32 s47, s43, 0
	global_load_dwordx4 v[174:177], v226, s[48:49]
	s_waitcnt lgkmcnt(9)
	v_mfma_f32_32x32x16_bf16 v[130:145], v[246:249], v[146:149], v[130:145]
	v_cvt_pk_bf16_f32 v70, v98, v99
	v_cvt_pk_bf16_f32 v71, v100, v101
	v_cvt_pk_bf16_f32 v72, v102, v103
	v_cvt_pk_bf16_f32 v73, v104, v105
	v_permlane32_swap_b32_e32 v228, v229
	global_load_dwordx4 v[8:11], v225, s[46:47]
	global_load_dwordx4 v[4:7], v225, s[46:47] offset:128
	s_waitcnt lgkmcnt(8)
	v_mfma_f32_32x32x16_bf16 v[114:129], v[250:253], v[146:149], v[114:129]
	v_cvt_pk_bf16_f32 v12, v106, v107
	v_cvt_pk_bf16_f32 v13, v108, v109
	v_cvt_pk_bf16_f32 v14, v110, v111
	v_cvt_pk_bf16_f32 v15, v112, v113
	ds_read_b64_tr_b16 v[78:79], v213 offset:41472
	ds_read_b64_tr_b16 v[80:81], v213 offset:42496
	ds_read_b64_tr_b16 v[98:99], v213 offset:43520
	ds_read_b64_tr_b16 v[100:101], v213 offset:44544
	ds_read_b64_tr_b16 v[102:103], v213 offset:45568
	ds_read_b64_tr_b16 v[104:105], v213 offset:46592
	ds_read_b64_tr_b16 v[110:111], v213 offset:47616
	ds_read_b64_tr_b16 v[112:113], v213 offset:48640
	v_max3_f32 v2, v130, v131, v132
	v_max3_f32 v2, v2, v133, v134
	v_max3_f32 v2, v2, v135, v136
	v_max3_f32 v2, v2, v137, v138
	v_max3_f32 v2, v2, v139, v140
	v_max3_f32 v2, v2, v141, v142
	v_max3_f32 v2, v2, v143, v144
	v_max3_f32 v2, v2, v145, v114
	v_max3_f32 v2, v2, v115, v116
	s_waitcnt lgkmcnt(8)
	v_mfma_f32_32x32x16_bf16 v[50:65], v[230:233], v[74:77], v[50:65]
	v_max3_f32 v2, v2, v117, v118
	v_max3_f32 v2, v2, v119, v120
	v_max3_f32 v2, v2, v121, v122
	v_mfma_f32_32x32x16_bf16 v[50:65], v[234:237], v[66:69], v[50:65]
	v_max3_f32 v2, v2, v123, v124
	v_max3_f32 v2, v2, v125, v126
	v_max3_f32 v2, v2, v127, v128
	v_mfma_f32_32x32x16_bf16 v[50:65], v[238:241], v[70:73], v[50:65]
	v_max_f32_e32 v2, v2, v129
	s_nop 0
	s_nop 0
	v_mfma_f32_32x32x16_bf16 v[50:65], v[242:245], v[12:15], v[50:65]
	v_mov_b32_e32 v16, v2
	s_nop 1
	v_permlane32_swap_b32_e32 v2, v16
	v_max_f32_e32 v2, v2, v16
	v_cmp_ge_f32_e32 vcc, s28, v2
	s_cmp_eq_u64 vcc, exec
	s_cbranch_scc0 .LBB0_542_1
	v_mov_b32_e32 v2, 1.0
.LBB0_527_1:
	s_waitcnt lgkmcnt(0)
	v_mfma_f32_32x32x16_bf16 v[34:49], v[78:81], v[74:77], v[34:49]
	s_waitcnt vmcnt(3)
	ds_write_b128 v187, v[178:181] offset:20480
	ds_write_b128 v214, v[182:185] offset:32768
	s_cmp_eq_u64 s[2:3], 0
	s_cbranch_scc1 .Lmla_a_nokr_1
	ds_write_b128 v216, v[170:173] offset:28672

; #define SBAR() __builtin_amdgcn_sched_barrier(0)
; #define SLOAD(i, j) do { const int _row = KROW(j); skn[i] = *(const bf16x8*)(Knp + (size_t)(_row + sr) * ldk + c8 * 8); sv[i] = *(const bf16x8*)(Vp + (size_t)(_row + sr) * ldv + c8 * 8); \
;         if (krw) skr[i] = *(const bf16x8*)(Krp + (size_t)(_row + sr2) * 32 + c4 * 8); } while (0)
; #define SWRITEO(boff, i) do { *(LAS bf16x8*)(lds + (boff) + kn_st) = skn[i]; *(LAS bf16x8*)(lds + (boff) + v_stw) = sv[i]; if (krw) *(LAS bf16x8*)(lds + (boff) + kr_st) = skr[i]; } while (0)
; #define PVO(boff) do { pv_one<0>(o0, vb0 + (boff), pa0, pa1, pa2, pa3); pv_one<1>(o1, vb0 + (boff), pa0, pa1, pa2, pa3); } while (0)
; #define SWAIT() asm volatile("s_waitcnt vmcnt(2)" ::: "memory")
; #define RESC(a) do { if (__any((a) < 1.f)) { _Pragma("unroll") for (int r = 0; r < 16; ++r) { o0[r] *= (a); o1[r] *= (a); } } } while (0)
; #define ROT() do { const int _t = bV; bV = bK; bK = bW; bW = _t; } while (0)
; template <int D0> __device__ __forceinline__ void pv_one(f32x16& od, unsigned vb, bf16x8 pa0, bf16x8 pa1, bf16x8 pa2, bf16x8 pa3) {
;     const s16x4 l0 = tr_read<v_rd_off(D0, 0, 0)>(vb), h0 = tr_read<v_rd_off(D0, 0, 1)>(vb), l1 = tr_read<v_rd_off(D0, 1, 0)>(vb), h1 = tr_read<v_rd_off(D0, 1, 1)>(vb);
;     const s16x4 l2 = tr_read<v_rd_off(D0, 2, 0)>(vb), h2 = tr_read<v_rd_off(D0, 2, 1)>(vb), l3 = tr_read<v_rd_off(D0, 3, 0)>(vb), h3 = tr_read<v_rd_off(D0, 3, 1)>(vb);
;     asm volatile("s_waitcnt lgkmcnt(0)" ::: "memory"); SBAR();
;     ...
;     od = __builtin_amdgcn_mfma_f32_32x32x16_bf16(ATT_PK(l0, h0), pa0, od, 0, 0, 0);
;     od = __builtin_amdgcn_mfma_f32_32x32x16_bf16(ATT_PK(l1, h1), pa1, od, 0, 0, 0);
;     od = __builtin_amdgcn_mfma_f32_32x32x16_bf16(ATT_PK(l2, h2), pa2, od, 0, 0, 0);
;     od = __builtin_amdgcn_mfma_f32_32x32x16_bf16(ATT_PK(l3, h3), pa3, od, 0, 0, 0);
;     ...
; }
; template <int DQK, bool FIXM> ...
;     ...
;         if (!NOBAR_PROBE) __syncthreads();
;         SBAR(); qkt<DQK>(pA0, pA1, lds + bK, qr, r32, hi, negm);
;         finishSM(pB0, pB1, alB, l_reg, pa0, pa1, pa2, pa3); SBAR();
;         if (j + 3 < NT) SLOAD(0, j + 3); SBAR();
;         if constexpr (FIXM) pv_psm<true>(o0, o1, vb0 + bV, pa0, pa1, pa2, pa3, pA0, pA1, m_reg, negm, alA); else { PVO(bV); partialSM<false>(pA0, pA1, m_reg, negm, alA); }
;         SWAIT(); SWRITEO(bW, 1);
;         if (!FIXM) RESC(alA); ROT();
.LBB0_531_1:
	s_waitcnt lgkmcnt(0)
	s_barrier
	ds_read_b128 v[178:181], v209 offset:20480
	ds_read_b128 v[182:185], v209 offset:24576
	ds_read_b128 v[170:173], v210 offset:20480
	ds_read_b128 v[66:69], v210 offset:24576
	ds_read_b128 v[70:73], v211 offset:20480
	ds_read_b128 v[74:77], v211 offset:24576
	ds_read_b128 v[78:81], v212 offset:20480
	v_exp_f32_e32 v114, v114
	v_exp_f32_e32 v115, v115
	v_exp_f32_e32 v116, v116
	v_exp_f32_e32 v117, v117
	v_exp_f32_e32 v118, v118
	v_exp_f32_e32 v119, v119
	v_exp_f32_e32 v120, v120
	v_exp_f32_e32 v121, v121
	s_waitcnt lgkmcnt(6)
	v_mfma_f32_32x32x16_bf16 v[130:145], v[178:181], v[166:169], v[82:97]
	ds_read_b128 v[178:181], v212 offset:24576
	v_exp_f32_e32 v122, v122
	v_exp_f32_e32 v123, v123
	v_exp_f32_e32 v124, v124
	v_cvt_pk_bf16_f32 v12, v16, v234
	s_waitcnt lgkmcnt(6)
	v_mfma_f32_32x32x16_bf16 v[98:113], v[182:185], v[166:169], v[82:97]
	ds_read_b128 v[182:185], v219 offset:28672
	v_exp_f32_e32 v125, v125
	v_exp_f32_e32 v126, v126
	v_exp_f32_e32 v127, v127
	v_cvt_pk_bf16_f32 v13, v235, v236
	s_waitcnt lgkmcnt(6)
	v_mfma_f32_32x32x16_bf16 v[130:145], v[170:173], v[162:165], v[130:145]
	ds_read_b128 v[170:173], v219 offset:30720
	v_exp_f32_e32 v128, v128
	v_exp_f32_e32 v129, v129
	v_cvt_pk_bf16_f32 v14, v237, v238
	v_cvt_pk_bf16_f32 v15, v239, v240
	v_add_f32_e32 v252, 0, v16
	v_add_f32_e32 v252, v234, v252
	s_waitcnt lgkmcnt(6)
	v_mfma_f32_32x32x16_bf16 v[98:113], v[66:69], v[162:165], v[98:113]
	ds_read_b128 v[66:69], v220 offset:28672
	v_cvt_pk_bf16_f32 v230, v241, v242
	v_cvt_pk_bf16_f32 v231, v243, v244
	v_add_f32_e32 v252, v235, v252
	v_add_f32_e32 v252, v236, v252
	v_add_f32_e32 v252, v237, v252
	v_add_f32_e32 v252, v238, v252
	s_waitcnt lgkmcnt(6)
	v_mfma_f32_32x32x16_bf16 v[130:145], v[70:73], v[158:161], v[130:145]
	ds_read_b128 v[70:73], v220 offset:30720
	v_cvt_pk_bf16_f32 v232, v245, v246
	v_cvt_pk_bf16_f32 v233, v247, v248
	v_add_f32_e32 v252, v239, v252
	v_add_f32_e32 v252, v240, v252
	v_add_f32_e32 v252, v241, v252
	v_add_f32_e32 v252, v242, v252
	s_waitcnt lgkmcnt(6)
	v_mfma_f32_32x32x16_bf16 v[98:113], v[74:77], v[158:161], v[98:113]
	v_add_f32_e32 v252, v243, v252
	v_add_f32_e32 v252, v244, v252
	v_add_f32_e32 v252, v245, v252
	v_add_f32_e32 v252, v246, v252
	v_add_f32_e32 v252, v247, v252
	v_add_f32_e32 v252, v248, v252
	s_waitcnt lgkmcnt(5)
	v_mfma_f32_32x32x16_bf16 v[130:145], v[78:81], v[154:157], v[130:145]
	ds_read_b64_tr_b16 v[234:235], v213 offset:0
	ds_read_b64_tr_b16 v[236:237], v213 offset:1024
	ds_read_b64_tr_b16 v[238:239], v213 offset:2048
	ds_read_b64_tr_b16 v[240:241], v213 offset:3072
	v_add_f32_e32 v252, v114, v252
	v_add_f32_e32 v252, v115, v252
	v_add_f32_e32 v252, v116, v252
	s_waitcnt lgkmcnt(8)
	v_mfma_f32_32x32x16_bf16 v[98:113], v[178:181], v[154:157], v[98:113]
	ds_read_b64_tr_b16 v[242:243], v213 offset:4096
	ds_read_b64_tr_b16 v[244:245], v213 offset:5120
	ds_read_b64_tr_b16 v[246:247], v213 offset:6144
	ds_read_b64_tr_b16 v[248:249], v213 offset:7168
	v_add_f32_e32 v252, v117, v252
	v_add_f32_e32 v252, v118, v252
	v_add_f32_e32 v252, v119, v252
	s_waitcnt lgkmcnt(11)
	v_mfma_f32_32x32x16_bf16 v[130:145], v[182:185], v[150:153], v[130:145]
	v_add_f32_e32 v252, v120, v252
	v_add_f32_e32 v252, v121, v252
	v_add_f32_e32 v252, v122, v252
	v_add_f32_e32 v252, v123, v252
	v_add_f32_e32 v252, v124, v252
	v_add_f32_e32 v252, v125, v252
	s_waitcnt lgkmcnt(10)
	v_mfma_f32_32x32x16_bf16 v[98:113], v[170:173], v[150:153], v[98:113]
	v_add_f32_e32 v252, v126, v252
	v_add_f32_e32 v252, v127, v252
	v_add_f32_e32 v252, v128, v252
	s_waitcnt lgkmcnt(9)
	v_mfma_f32_32x32x16_bf16 v[130:145], v[66:69], v[146:149], v[130:145]
	v_cvt_pk_bf16_f32 v114, v114, v115
	v_cvt_pk_bf16_f32 v115, v116, v117
	v_cvt_pk_bf16_f32 v116, v118, v119
	v_cvt_pk_bf16_f32 v117, v120, v121
	s_cmp_ge_u32 s35, s31
	s_cbranch_scc1 .Lmla_b_noload_1
	s_cmp_lt_u32 s35, s30
	s_cselect_b32 s0, 0, s30
	s_cselect_b32 s1, s29, s34
	s_lshl_b32 s0, s0, 6
	s_sub_i32 s37, s1, s0
	s_lshl_b32 s1, s35, 6
	s_add_i32 s37, s37, s1
	s_lshl_b32 s0, s37, 6
	s_add_u32 s48, s44, s0
	s_addc_u32 s49, s45, 0
	s_lshl_b32 s0, s37, 11
	s_add_u32 s46, s42, s0
	s_addc_u32 s47, s43, 0
	global_load_dwordx4 v[170:173], v226, s[48:49]
	global_load_dwordx4 v[178:181], v225, s[46:47]
	global_load_dwordx4 v[182:185], v225, s[46:47] offset:128
.Lmla_b_ld_done_1:
	s_waitcnt lgkmcnt(8)
	v_mfma_f32_32x32x16_bf16 v[98:113], v[70:73], v[146:149], v[98:113]
	v_cvt_pk_bf16_f32 v118, v122, v123
	v_cvt_pk_bf16_f32 v119, v124, v125
	v_cvt_pk_bf16_f32 v120, v126, v127
	v_cvt_pk_bf16_f32 v121, v128, v129
	v_add_f32_e32 v126, v129, v252
	v_mov_b32_e32 v127, v126
	ds_read_b64_tr_b16 v[66:67], v213 offset:512
	ds_read_b64_tr_b16 v[68:69], v213 offset:1536
	ds_read_b64_tr_b16 v[70:71], v213 offset:2560
	ds_read_b64_tr_b16 v[72:73], v213 offset:3584
	ds_read_b64_tr_b16 v[74:75], v213 offset:4608
	ds_read_b64_tr_b16 v[76:77], v213 offset:5632
	ds_read_b64_tr_b16 v[78:79], v213 offset:6656
	ds_read_b64_tr_b16 v[80:81], v213 offset:7680
	v_permlane32_swap_b32_e32 v126, v127
	v_max3_f32 v250, v130, v131, v132
	v_max3_f32 v250, v250, v133, v134
	v_max3_f32 v250, v250, v135, v136
	v_max3_f32 v250, v250, v137, v138
	v_max3_f32 v250, v250, v139, v140
	v_max3_f32 v250, v250, v141, v142
	v_max3_f32 v250, v250, v143, v144
	v_max3_f32 v250, v250, v145, v98
	v_max3_f32 v250, v250, v99, v100
	s_waitcnt lgkmcnt(8)
	v_mfma_f32_32x32x16_bf16 v[50:65], v[234:237], v[12:15], v[50:65]
	v_max3_f32 v250, v250, v101, v102
	v_max3_f32 v250, v250, v103, v104
	v_max3_f32 v250, v250, v105, v106
	v_mfma_f32_32x32x16_bf16 v[50:65], v[238:241], v[230:233], v[50:65]
	v_max3_f32 v250, v250, v107, v108
	v_max3_f32 v250, v250, v109, v110
	v_max3_f32 v250, v250, v111, v112
	v_mfma_f32_32x32x16_bf16 v[50:65], v[242:245], v[114:117], v[50:65]
	v_max_f32_e32 v250, v250, v113
	s_nop 0
	s_nop 0
	v_mfma_f32_32x32x16_bf16 v[50:65], v[246:249], v[118:121], v[50:65]
	v_mov_b32_e32 v251, v250
	s_nop 1
	v_permlane32_swap_b32_e32 v250, v251
	v_max_f32_e32 v250, v250, v251
	v_cmp_ge_f32_e32 vcc, s28, v250
	s_cmp_eq_u64 vcc, exec
	v_mov_b32_e32 v16, 1.0
	s_cbranch_scc0 .LBB0_543_1
.LBB0_536_1:
	s_waitcnt lgkmcnt(0)
	v_mfma_f32_32x32x16_bf16 v[34:49], v[66:69], v[12:15], v[34:49]
	s_waitcnt vmcnt(3)
	ds_write_b128 v187, v[8:11] offset:40960
	ds_write_b128 v214, v[4:7] offset:53248
	s_cmp_eq_u64 s[2:3], 0
	s_cbranch_scc1 .Lmla_b_nokr_1
	ds_write_b128 v216, v[174:177] offset:49152

; #define SBAR() __builtin_amdgcn_sched_barrier(0)
; #define ATT_PKN(P, BASE, OUT) do { u32x4 w = {cvt_pk_bf16(P[BASE + 0], P[BASE + 1]), cvt_pk_bf16(P[BASE + 2], P[BASE + 3]), cvt_pk_bf16(P[BASE + 4], P[BASE + 5]), cvt_pk_bf16(P[BASE + 6], P[BASE + 7])}; \
;     OUT = __builtin_bit_cast(bf16x8, w); } while (0)
; #define SLOAD(i, j) do { const int _row = KROW(j); skn[i] = *(const bf16x8*)(Knp + (size_t)(_row + sr) * ldk + c8 * 8); sv[i] = *(const bf16x8*)(Vp + (size_t)(_row + sr) * ldv + c8 * 8); \
;         if (krw) skr[i] = *(const bf16x8*)(Krp + (size_t)(_row + sr2) * 32 + c4 * 8); } while (0)
; #define SWRITEO(boff, i) do { *(LAS bf16x8*)(lds + (boff) + kn_st) = skn[i]; *(LAS bf16x8*)(lds + (boff) + v_stw) = sv[i]; if (krw) *(LAS bf16x8*)(lds + (boff) + kr_st) = skr[i]; } while (0)
; #define PVO(boff) do { pv_one<0>(o0, vb0 + (boff), pa0, pa1, pa2, pa3); pv_one<1>(o1, vb0 + (boff), pa0, pa1, pa2, pa3); } while (0)
; #define SWAIT() asm volatile("s_waitcnt vmcnt(2)" ::: "memory")
; #define ROT() do { const int _t = bV; bV = bK; bK = bW; bW = _t; } while (0)
; __device__ __forceinline__ void finishSM(f32x16& p0, f32x16& p1, float alpha, float& l_reg, bf16x8& pa0, bf16x8& pa1, bf16x8& pa2, bf16x8& pa3) {
; #pragma unroll
;     for (int r = 0; r < 16; ++r) p1[r] = EXP_PROBE ? fmaf(p1[r], 0.001f, 1.f) : __builtin_amdgcn_exp2f(p1[r]);
;     float ps = 0.f;
; #pragma unroll
;     for (int r = 0; r < 16; ++r) ps += p0[r];
; #pragma unroll
;     for (int r = 0; r < 16; ++r) ps += p1[r];
;     { auto rr = __builtin_amdgcn_permlane32_swap(__float_as_uint(ps), __float_as_uint(ps), false, false);
;       ps = __uint_as_float(rr[0]) + __uint_as_float(rr[1]); }
;     l_reg = l_reg * alpha + ps;
;     ATT_PKN(p0, 0, pa0); ATT_PKN(p0, 8, pa1); ATT_PKN(p1, 0, pa2); ATT_PKN(p1, 8, pa3);
; }
; template <int DQK, bool FIXM> ...
;     ...
;     for (int j = 1; j + 1 < NT; j += 2) {
;         if (!NOBAR_PROBE) __syncthreads();
;         SBAR(); qkt<DQK>(pB0, pB1, lds + bK, qr, r32, hi, negm);
;         finishSM(pA0, pA1, alA, l_reg, pa0, pa1, pa2, pa3); SBAR();
;         SLOAD(1, j + 2); SBAR();
;         if constexpr (FIXM) pv_psm<true>(o0, o1, vb0 + bV, pa0, pa1, pa2, pa3, pB0, pB1, m_reg, negm, alB); else { PVO(bV); partialSM<false>(pB0, pB1, m_reg, negm, alB); }
;         SWAIT(); SWRITEO(bW, 0);
;         if (!FIXM) RESC(alB); ROT();
.LBB0_540_1:
	v_add_f32_e32 v4, v228, v229
	v_fmac_f32_e32 v4, v227, v223
	v_add_f32_e32 v223, v126, v127
	s_add_i32 s35, s35, 2
	v_fmac_f32_e32 v223, v4, v2
	s_cmp_ge_u32 s36, s12
	s_cbranch_scc1 .Lmla_exit_1
	v_mov_b32_e32 v227, v16
	s_waitcnt lgkmcnt(0)
	s_barrier
	ds_read_b128 v[4:7], v209 offset:40960
	ds_read_b128 v[8:11], v209 offset:45056
	ds_read_b128 v[174:177], v210 offset:40960
	ds_read_b128 v[246:249], v210 offset:45056
	ds_read_b128 v[250:253], v211 offset:40960
	ds_read_b128 v[78:81], v211 offset:45056
	ds_read_b128 v[12:15], v212 offset:40960
	v_exp_f32_e32 v98, v98
	v_exp_f32_e32 v99, v99
	v_exp_f32_e32 v100, v100
	v_exp_f32_e32 v101, v101
	v_exp_f32_e32 v102, v102
	v_exp_f32_e32 v103, v103
	v_exp_f32_e32 v104, v104
	v_exp_f32_e32 v105, v105
	s_waitcnt lgkmcnt(6)
	v_mfma_f32_32x32x16_bf16 v[130:145], v[4:7], v[166:169], v[82:97]
	ds_read_b128 v[4:7], v212 offset:45056
	v_exp_f32_e32 v106, v106
	v_exp_f32_e32 v107, v107
	v_exp_f32_e32 v108, v108
	v_cvt_pk_bf16_f32 v74, v243, v245
	s_waitcnt lgkmcnt(6)
	v_mfma_f32_32x32x16_bf16 v[114:129], v[8:11], v[166:169], v[82:97]
	ds_read_b128 v[8:11], v219 offset:49152
	v_exp_f32_e32 v109, v109
	v_exp_f32_e32 v110, v110
	v_exp_f32_e32 v111, v111
	v_cvt_pk_bf16_f32 v75, v241, v244
	s_waitcnt lgkmcnt(6)
	v_mfma_f32_32x32x16_bf16 v[130:145], v[174:177], v[162:165], v[130:145]
	ds_read_b128 v[174:177], v219 offset:51200
	v_exp_f32_e32 v112, v112
	v_exp_f32_e32 v113, v113
	v_cvt_pk_bf16_f32 v76, v239, v242
	v_cvt_pk_bf16_f32 v77, v238, v240
	v_add_f32_e32 v229, 0, v243
	v_add_f32_e32 v229, v245, v229
	s_waitcnt lgkmcnt(6)
	v_mfma_f32_32x32x16_bf16 v[114:129], v[246:249], v[162:165], v[114:129]
	ds_read_b128 v[246:249], v220 offset:49152
	v_cvt_pk_bf16_f32 v66, v236, v237
	v_cvt_pk_bf16_f32 v67, v233, v235
	v_add_f32_e32 v229, v241, v229
	v_add_f32_e32 v229, v244, v229
	v_add_f32_e32 v229, v239, v229
	v_add_f32_e32 v229, v242, v229
	s_waitcnt lgkmcnt(6)
	v_mfma_f32_32x32x16_bf16 v[130:145], v[250:253], v[158:161], v[130:145]
	ds_read_b128 v[250:253], v220 offset:51200
	v_cvt_pk_bf16_f32 v68, v231, v234
	v_cvt_pk_bf16_f32 v69, v230, v232
	v_add_f32_e32 v229, v238, v229
	v_add_f32_e32 v229, v240, v229
	v_add_f32_e32 v229, v236, v229
	v_add_f32_e32 v229, v237, v229
	s_waitcnt lgkmcnt(6)
	v_mfma_f32_32x32x16_bf16 v[114:129], v[78:81], v[158:161], v[114:129]
	v_add_f32_e32 v229, v233, v229
	v_add_f32_e32 v229, v235, v229
	v_add_f32_e32 v229, v231, v229
	v_add_f32_e32 v229, v234, v229
	v_add_f32_e32 v229, v230, v229
	v_add_f32_e32 v229, v232, v229
	s_waitcnt lgkmcnt(5)
	v_mfma_f32_32x32x16_bf16 v[130:145], v[12:15], v[154:157], v[130:145]
	ds_read_b64_tr_b16 v[230:231], v213 offset:20480
	ds_read_b64_tr_b16 v[232:233], v213 offset:21504
	ds_read_b64_tr_b16 v[234:235], v213 offset:22528
	ds_read_b64_tr_b16 v[236:237], v213 offset:23552
	v_add_f32_e32 v229, v98, v229
	v_add_f32_e32 v229, v99, v229
	v_add_f32_e32 v229, v100, v229
	s_waitcnt lgkmcnt(8)
	v_mfma_f32_32x32x16_bf16 v[114:129], v[4:7], v[154:157], v[114:129]
	ds_read_b64_tr_b16 v[238:239], v213 offset:24576
	ds_read_b64_tr_b16 v[240:241], v213 offset:25600
	ds_read_b64_tr_b16 v[242:243], v213 offset:26624
	ds_read_b64_tr_b16 v[244:245], v213 offset:27648
	v_add_f32_e32 v229, v101, v229
	v_add_f32_e32 v229, v102, v229
	v_add_f32_e32 v229, v103, v229
	s_waitcnt lgkmcnt(11)
	v_mfma_f32_32x32x16_bf16 v[130:145], v[8:11], v[150:153], v[130:145]
	v_add_f32_e32 v229, v104, v229
	v_add_f32_e32 v229, v105, v229
	v_add_f32_e32 v229, v106, v229
	v_add_f32_e32 v229, v107, v229
	v_add_f32_e32 v229, v108, v229
	v_add_f32_e32 v229, v109, v229
	s_waitcnt lgkmcnt(10)
	v_mfma_f32_32x32x16_bf16 v[114:129], v[174:177], v[150:153], v[114:129]
	v_add_f32_e32 v229, v110, v229
	v_add_f32_e32 v229, v111, v229
	v_add_f32_e32 v229, v112, v229
	v_add_f32_e32 v228, v113, v229
	v_mov_b32_e32 v229, v228
	s_add_i32 s36, s35, -1
	s_cmp_lt_u32 s36, s30
	s_cselect_b32 s0, 0, s30
	s_cselect_b32 s1, s29, s34
	s_lshl_b32 s0, s0, 6
	s_sub_i32 s37, s1, s0
	s_lshl_b32 s1, s36, 6
	s_add_i32 s37, s37, s1
	s_lshl_b32 s0, s37, 6
	s_add_u32 s48, s44, s0
	s_addc_u32 s49, s45, 0
	s_lshl_b32 s0, s37, 11
	s_add_u32 s46, s42, s0
	s_addc_u32 s47, s43, 0
	global_load_dwordx4 v[174:177], v226, s[48:49]
	s_waitcnt lgkmcnt(9)
	v_mfma_f32_32x32x16_bf16 v[130:145], v[246:249], v[146:149], v[130:145]
	v_cvt_pk_bf16_f32 v70, v98, v99
	v_cvt_pk_bf16_f32 v71, v100, v101
	v_cvt_pk_bf16_f32 v72, v102, v103
	v_cvt_pk_bf16_f32 v73, v104, v105
	v_permlane32_swap_b32_e32 v228, v229
	global_load_dwordx4 v[8:11], v225, s[46:47]
	global_load_dwordx4 v[4:7], v225, s[46:47] offset:128
	s_waitcnt lgkmcnt(8)
	v_mfma_f32_32x32x16_bf16 v[114:129], v[250:253], v[146:149], v[114:129]
	v_cvt_pk_bf16_f32 v12, v106, v107
	v_cvt_pk_bf16_f32 v13, v108, v109
	v_cvt_pk_bf16_f32 v14, v110, v111
	v_cvt_pk_bf16_f32 v15, v112, v113
	ds_read_b64_tr_b16 v[78:79], v213 offset:20992
	ds_read_b64_tr_b16 v[80:81], v213 offset:22016
	ds_read_b64_tr_b16 v[98:99], v213 offset:23040
	ds_read_b64_tr_b16 v[100:101], v213 offset:24064
	ds_read_b64_tr_b16 v[102:103], v213 offset:25088
	ds_read_b64_tr_b16 v[104:105], v213 offset:26112
	ds_read_b64_tr_b16 v[110:111], v213 offset:27136
	ds_read_b64_tr_b16 v[112:113], v213 offset:28160
	v_max3_f32 v2, v130, v131, v132
	v_max3_f32 v2, v2, v133, v134
	v_max3_f32 v2, v2, v135, v136
	v_max3_f32 v2, v2, v137, v138
	v_max3_f32 v2, v2, v139, v140
	v_max3_f32 v2, v2, v141, v142
	v_max3_f32 v2, v2, v143, v144
	v_max3_f32 v2, v2, v145, v114
	v_max3_f32 v2, v2, v115, v116
	s_waitcnt lgkmcnt(8)
	v_mfma_f32_32x32x16_bf16 v[50:65], v[230:233], v[74:77], v[50:65]
	v_max3_f32 v2, v2, v117, v118
	v_max3_f32 v2, v2, v119, v120
	v_max3_f32 v2, v2, v121, v122
	v_mfma_f32_32x32x16_bf16 v[50:65], v[234:237], v[66:69], v[50:65]
	v_max3_f32 v2, v2, v123, v124
	v_max3_f32 v2, v2, v125, v126
	v_max3_f32 v2, v2, v127, v128
	v_mfma_f32_32x32x16_bf16 v[50:65], v[238:241], v[70:73], v[50:65]
	v_max_f32_e32 v2, v2, v129
	s_nop 0
	s_nop 0
	v_mfma_f32_32x32x16_bf16 v[50:65], v[242:245], v[12:15], v[50:65]
	v_mov_b32_e32 v16, v2
	s_nop 1
	v_permlane32_swap_b32_e32 v2, v16
	v_max_f32_e32 v2, v2, v16
	v_cmp_ge_f32_e32 vcc, s28, v2
	s_cmp_eq_u64 vcc, exec
	s_cbranch_scc0 .LBB0_542_2
	v_mov_b32_e32 v2, 1.0
.LBB0_527_2:
	s_waitcnt lgkmcnt(0)
	v_mfma_f32_32x32x16_bf16 v[34:49], v[78:81], v[74:77], v[34:49]
	s_waitcnt vmcnt(3)
	ds_write_b128 v187, v[178:181] offset:0
	ds_write_b128 v214, v[182:185] offset:12288
	s_cmp_eq_u64 s[2:3], 0
	s_cbranch_scc1 .Lmla_a_nokr_2
	ds_write_b128 v216, v[170:173] offset:8192

; #define SBAR() __builtin_amdgcn_sched_barrier(0)
; #define SLOAD(i, j) do { const int _row = KROW(j); skn[i] = *(const bf16x8*)(Knp + (size_t)(_row + sr) * ldk + c8 * 8); sv[i] = *(const bf16x8*)(Vp + (size_t)(_row + sr) * ldv + c8 * 8); \
;         if (krw) skr[i] = *(const bf16x8*)(Krp + (size_t)(_row + sr2) * 32 + c4 * 8); } while (0)
; #define SWRITEO(boff, i) do { *(LAS bf16x8*)(lds + (boff) + kn_st) = skn[i]; *(LAS bf16x8*)(lds + (boff) + v_stw) = sv[i]; if (krw) *(LAS bf16x8*)(lds + (boff) + kr_st) = skr[i]; } while (0)
; #define PVO(boff) do { pv_one<0>(o0, vb0 + (boff), pa0, pa1, pa2, pa3); pv_one<1>(o1, vb0 + (boff), pa0, pa1, pa2, pa3); } while (0)
; #define SWAIT() asm volatile("s_waitcnt vmcnt(2)" ::: "memory")
; #define RESC(a) do { if (__any((a) < 1.f)) { _Pragma("unroll") for (int r = 0; r < 16; ++r) { o0[r] *= (a); o1[r] *= (a); } } } while (0)
; #define ROT() do { const int _t = bV; bV = bK; bK = bW; bW = _t; } while (0)
; template <int D0> __device__ __forceinline__ void pv_one(f32x16& od, unsigned vb, bf16x8 pa0, bf16x8 pa1, bf16x8 pa2, bf16x8 pa3) {
;     const s16x4 l0 = tr_read<v_rd_off(D0, 0, 0)>(vb), h0 = tr_read<v_rd_off(D0, 0, 1)>(vb), l1 = tr_read<v_rd_off(D0, 1, 0)>(vb), h1 = tr_read<v_rd_off(D0, 1, 1)>(vb);
;     const s16x4 l2 = tr_read<v_rd_off(D0, 2, 0)>(vb), h2 = tr_read<v_rd_off(D0, 2, 1)>(vb), l3 = tr_read<v_rd_off(D0, 3, 0)>(vb), h3 = tr_read<v_rd_off(D0, 3, 1)>(vb);
;     asm volatile("s_waitcnt lgkmcnt(0)" ::: "memory"); SBAR();
;     ...
;     od = __builtin_amdgcn_mfma_f32_32x32x16_bf16(ATT_PK(l0, h0), pa0, od, 0, 0, 0);
;     od = __builtin_amdgcn_mfma_f32_32x32x16_bf16(ATT_PK(l1, h1), pa1, od, 0, 0, 0);
;     od = __builtin_amdgcn_mfma_f32_32x32x16_bf16(ATT_PK(l2, h2), pa2, od, 0, 0, 0);
;     od = __builtin_amdgcn_mfma_f32_32x32x16_bf16(ATT_PK(l3, h3), pa3, od, 0, 0, 0);
;     ...
; }
; template <int DQK, bool FIXM> ...
;     ...
;         if (!NOBAR_PROBE) __syncthreads();
;         SBAR(); qkt<DQK>(pA0, pA1, lds + bK, qr, r32, hi, negm);
;         finishSM(pB0, pB1, alB, l_reg, pa0, pa1, pa2, pa3); SBAR();
;         if (j + 3 < NT) SLOAD(0, j + 3); SBAR();
;         if constexpr (FIXM) pv_psm<true>(o0, o1, vb0 + bV, pa0, pa1, pa2, pa3, pA0, pA1, m_reg, negm, alA); else { PVO(bV); partialSM<false>(pA0, pA1, m_reg, negm, alA); }
;         SWAIT(); SWRITEO(bW, 1);
;         if (!FIXM) RESC(alA); ROT();
.LBB0_531_2:
	s_waitcnt lgkmcnt(0)
	s_barrier
	ds_read_b128 v[178:181], v209 offset:0
	ds_read_b128 v[182:185], v209 offset:4096
	ds_read_b128 v[170:173], v210 offset:0
	ds_read_b128 v[66:69], v210 offset:4096
	ds_read_b128 v[70:73], v211 offset:0
	ds_read_b128 v[74:77], v211 offset:4096
	ds_read_b128 v[78:81], v212 offset:0
	v_exp_f32_e32 v114, v114
	v_exp_f32_e32 v115, v115
	v_exp_f32_e32 v116, v116
	v_exp_f32_e32 v117, v117
	v_exp_f32_e32 v118, v118
	v_exp_f32_e32 v119, v119
	v_exp_f32_e32 v120, v120
	v_exp_f32_e32 v121, v121
	s_waitcnt lgkmcnt(6)
	v_mfma_f32_32x32x16_bf16 v[130:145], v[178:181], v[166:169], v[82:97]
	ds_read_b128 v[178:181], v212 offset:4096
	v_exp_f32_e32 v122, v122
	v_exp_f32_e32 v123, v123
	v_exp_f32_e32 v124, v124
	v_cvt_pk_bf16_f32 v12, v16, v234
	s_waitcnt lgkmcnt(6)
	v_mfma_f32_32x32x16_bf16 v[98:113], v[182:185], v[166:169], v[82:97]
	ds_read_b128 v[182:185], v219 offset:8192
	v_exp_f32_e32 v125, v125
	v_exp_f32_e32 v126, v126
	v_exp_f32_e32 v127, v127
	v_cvt_pk_bf16_f32 v13, v235, v236
	s_waitcnt lgkmcnt(6)
	v_mfma_f32_32x32x16_bf16 v[130:145], v[170:173], v[162:165], v[130:145]
	ds_read_b128 v[170:173], v219 offset:10240
	v_exp_f32_e32 v128, v128
	v_exp_f32_e32 v129, v129
	v_cvt_pk_bf16_f32 v14, v237, v238
	v_cvt_pk_bf16_f32 v15, v239, v240
	v_add_f32_e32 v252, 0, v16
	v_add_f32_e32 v252, v234, v252
	s_waitcnt lgkmcnt(6)
	v_mfma_f32_32x32x16_bf16 v[98:113], v[66:69], v[162:165], v[98:113]
	ds_read_b128 v[66:69], v220 offset:8192
	v_cvt_pk_bf16_f32 v230, v241, v242
	v_cvt_pk_bf16_f32 v231, v243, v244
	v_add_f32_e32 v252, v235, v252
	v_add_f32_e32 v252, v236, v252
	v_add_f32_e32 v252, v237, v252
	v_add_f32_e32 v252, v238, v252
	s_waitcnt lgkmcnt(6)
	v_mfma_f32_32x32x16_bf16 v[130:145], v[70:73], v[158:161], v[130:145]
	ds_read_b128 v[70:73], v220 offset:10240
	v_cvt_pk_bf16_f32 v232, v245, v246
	v_cvt_pk_bf16_f32 v233, v247, v248
	v_add_f32_e32 v252, v239, v252
	v_add_f32_e32 v252, v240, v252
	v_add_f32_e32 v252, v241, v252
	v_add_f32_e32 v252, v242, v252
	s_waitcnt lgkmcnt(6)
	v_mfma_f32_32x32x16_bf16 v[98:113], v[74:77], v[158:161], v[98:113]
	v_add_f32_e32 v252, v243, v252
	v_add_f32_e32 v252, v244, v252
	v_add_f32_e32 v252, v245, v252
	v_add_f32_e32 v252, v246, v252
	v_add_f32_e32 v252, v247, v252
	v_add_f32_e32 v252, v248, v252
	s_waitcnt lgkmcnt(5)
	v_mfma_f32_32x32x16_bf16 v[130:145], v[78:81], v[154:157], v[130:145]
	ds_read_b64_tr_b16 v[234:235], v213 offset:40960
	ds_read_b64_tr_b16 v[236:237], v213 offset:41984
	ds_read_b64_tr_b16 v[238:239], v213 offset:43008
	ds_read_b64_tr_b16 v[240:241], v213 offset:44032
	v_add_f32_e32 v252, v114, v252
	v_add_f32_e32 v252, v115, v252
	v_add_f32_e32 v252, v116, v252
	s_waitcnt lgkmcnt(8)
	v_mfma_f32_32x32x16_bf16 v[98:113], v[178:181], v[154:157], v[98:113]
	ds_read_b64_tr_b16 v[242:243], v213 offset:45056
	ds_read_b64_tr_b16 v[244:245], v213 offset:46080
	ds_read_b64_tr_b16 v[246:247], v213 offset:47104
	ds_read_b64_tr_b16 v[248:249], v213 offset:48128
	v_add_f32_e32 v252, v117, v252
	v_add_f32_e32 v252, v118, v252
	v_add_f32_e32 v252, v119, v252
	s_waitcnt lgkmcnt(11)
	v_mfma_f32_32x32x16_bf16 v[130:145], v[182:185], v[150:153], v[130:145]
	v_add_f32_e32 v252, v120, v252
	v_add_f32_e32 v252, v121, v252
	v_add_f32_e32 v252, v122, v252
	v_add_f32_e32 v252, v123, v252
	v_add_f32_e32 v252, v124, v252
	v_add_f32_e32 v252, v125, v252
	s_waitcnt lgkmcnt(10)
	v_mfma_f32_32x32x16_bf16 v[98:113], v[170:173], v[150:153], v[98:113]
	v_add_f32_e32 v252, v126, v252
	v_add_f32_e32 v252, v127, v252
	v_add_f32_e32 v252, v128, v252
	s_waitcnt lgkmcnt(9)
	v_mfma_f32_32x32x16_bf16 v[130:145], v[66:69], v[146:149], v[130:145]
	v_cvt_pk_bf16_f32 v114, v114, v115
	v_cvt_pk_bf16_f32 v115, v116, v117
	v_cvt_pk_bf16_f32 v116, v118, v119
	v_cvt_pk_bf16_f32 v117, v120, v121
	s_cmp_ge_u32 s35, s31
	s_cbranch_scc1 .Lmla_b_noload_2
	s_cmp_lt_u32 s35, s30
	s_cselect_b32 s0, 0, s30
	s_cselect_b32 s1, s29, s34
	s_lshl_b32 s0, s0, 6
	s_sub_i32 s37, s1, s0
	s_lshl_b32 s1, s35, 6
	s_add_i32 s37, s37, s1
	s_lshl_b32 s0, s37, 6
	s_add_u32 s48, s44, s0
	s_addc_u32 s49, s45, 0
	s_lshl_b32 s0, s37, 11
	s_add_u32 s46, s42, s0
	s_addc_u32 s47, s43, 0
	global_load_dwordx4 v[170:173], v226, s[48:49]
	global_load_dwordx4 v[178:181], v225, s[46:47]
	global_load_dwordx4 v[182:185], v225, s[46:47] offset:128
.Lmla_b_ld_done_2:
	s_waitcnt lgkmcnt(8)
	v_mfma_f32_32x32x16_bf16 v[98:113], v[70:73], v[146:149], v[98:113]
	v_cvt_pk_bf16_f32 v118, v122, v123
	v_cvt_pk_bf16_f32 v119, v124, v125
	v_cvt_pk_bf16_f32 v120, v126, v127
	v_cvt_pk_bf16_f32 v121, v128, v129
	v_add_f32_e32 v126, v129, v252
	v_mov_b32_e32 v127, v126
	ds_read_b64_tr_b16 v[66:67], v213 offset:41472
	ds_read_b64_tr_b16 v[68:69], v213 offset:42496
	ds_read_b64_tr_b16 v[70:71], v213 offset:43520
	ds_read_b64_tr_b16 v[72:73], v213 offset:44544
	ds_read_b64_tr_b16 v[74:75], v213 offset:45568
	ds_read_b64_tr_b16 v[76:77], v213 offset:46592
	ds_read_b64_tr_b16 v[78:79], v213 offset:47616
	ds_read_b64_tr_b16 v[80:81], v213 offset:48640
	v_permlane32_swap_b32_e32 v126, v127
	v_max3_f32 v250, v130, v131, v132
	v_max3_f32 v250, v250, v133, v134
	v_max3_f32 v250, v250, v135, v136
	v_max3_f32 v250, v250, v137, v138
	v_max3_f32 v250, v250, v139, v140
	v_max3_f32 v250, v250, v141, v142
	v_max3_f32 v250, v250, v143, v144
	v_max3_f32 v250, v250, v145, v98
	v_max3_f32 v250, v250, v99, v100
	s_waitcnt lgkmcnt(8)
	v_mfma_f32_32x32x16_bf16 v[50:65], v[234:237], v[12:15], v[50:65]
	v_max3_f32 v250, v250, v101, v102
	v_max3_f32 v250, v250, v103, v104
	v_max3_f32 v250, v250, v105, v106
	v_mfma_f32_32x32x16_bf16 v[50:65], v[238:241], v[230:233], v[50:65]
	v_max3_f32 v250, v250, v107, v108
	v_max3_f32 v250, v250, v109, v110
	v_max3_f32 v250, v250, v111, v112
	v_mfma_f32_32x32x16_bf16 v[50:65], v[242:245], v[114:117], v[50:65]
	v_max_f32_e32 v250, v250, v113
	s_nop 0
	s_nop 0
	v_mfma_f32_32x32x16_bf16 v[50:65], v[246:249], v[118:121], v[50:65]
	v_mov_b32_e32 v251, v250
	s_nop 1
	v_permlane32_swap_b32_e32 v250, v251
	v_max_f32_e32 v250, v250, v251
	v_cmp_ge_f32_e32 vcc, s28, v250
	s_cmp_eq_u64 vcc, exec
	v_mov_b32_e32 v16, 1.0
	s_cbranch_scc0 .LBB0_543_2
.LBB0_536_2:
	s_waitcnt lgkmcnt(0)
	v_mfma_f32_32x32x16_bf16 v[34:49], v[66:69], v[12:15], v[34:49]
	s_waitcnt vmcnt(3)
	ds_write_b128 v187, v[8:11] offset:20480
	ds_write_b128 v214, v[4:7] offset:32768
	s_cmp_eq_u64 s[2:3], 0
	s_cbranch_scc1 .Lmla_b_nokr_2
	ds_write_b128 v216, v[174:177] offset:28672

; #define SBAR() __builtin_amdgcn_sched_barrier(0)
; #define SLOAD(i, j) do { const int _row = KROW(j); skn[i] = *(const bf16x8*)(Knp + (size_t)(_row + sr) * ldk + c8 * 8); sv[i] = *(const bf16x8*)(Vp + (size_t)(_row + sr) * ldv + c8 * 8); \
;         if (krw) skr[i] = *(const bf16x8*)(Krp + (size_t)(_row + sr2) * 32 + c4 * 8); } while (0)
; #define SWRITEO(boff, i) do { *(LAS bf16x8*)(lds + (boff) + kn_st) = skn[i]; *(LAS bf16x8*)(lds + (boff) + v_stw) = sv[i]; if (krw) *(LAS bf16x8*)(lds + (boff) + kr_st) = skr[i]; } while (0)
; #define PVO(boff) do { pv_one<0>(o0, vb0 + (boff), pa0, pa1, pa2, pa3); pv_one<1>(o1, vb0 + (boff), pa0, pa1, pa2, pa3); } while (0)
; #define SWAIT() asm volatile("s_waitcnt vmcnt(2)" ::: "memory")
; #define RESC(a) do { if (__any((a) < 1.f)) { _Pragma("unroll") for (int r = 0; r < 16; ++r) { o0[r] *= (a); o1[r] *= (a); } } } while (0)
; #define ROT() do { const int _t = bV; bV = bK; bK = bW; bW = _t; } while (0)
; template <int DQK, bool FIXM> ...
;     ...
;     for (int j = 1; j + 1 < NT; j += 2) {
;         if (!NOBAR_PROBE) __syncthreads();
;         SBAR(); qkt<DQK>(pB0, pB1, lds + bK, qr, r32, hi, negm);
;         finishSM(pA0, pA1, alA, l_reg, pa0, pa1, pa2, pa3); SBAR();
;         SLOAD(1, j + 2); SBAR();
;         if constexpr (FIXM) pv_psm<true>(o0, o1, vb0 + bV, pa0, pa1, pa2, pa3, pB0, pB1, m_reg, negm, alB); else { PVO(bV); partialSM<false>(pB0, pB1, m_reg, negm, alB); }
;         SWAIT(); SWRITEO(bW, 0);
;         if (!FIXM) RESC(alB); ROT();
;         if (!NOBAR_PROBE) __syncthreads();
;         SBAR(); qkt<DQK>(pA0, pA1, lds + bK, qr, r32, hi, negm);
;         finishSM(pB0, pB1, alB, l_reg, pa0, pa1, pa2, pa3); SBAR();
;         if (j + 3 < NT) SLOAD(0, j + 3); SBAR();
;         if constexpr (FIXM) pv_psm<true>(o0, o1, vb0 + bV, pa0, pa1, pa2, pa3, pA0, pA1, m_reg, negm, alA); else { PVO(bV); partialSM<false>(pA0, pA1, m_reg, negm, alA); }
;         SWAIT(); SWRITEO(bW, 1);
;         if (!FIXM) RESC(alA); ROT();
;     }
.LBB0_540_2:
	v_add_f32_e32 v4, v228, v229
	v_fmac_f32_e32 v4, v227, v223
	v_add_f32_e32 v223, v126, v127
	s_add_i32 s35, s35, 2
	v_fmac_f32_e32 v223, v4, v2
	s_cmp_ge_u32 s36, s12
	s_cbranch_scc1 .Lmla_exit_2
	v_mov_b32_e32 v227, v16
	s_branch .LBB0_523

; #define SBAR() __builtin_amdgcn_sched_barrier(0)
; #define PVO(boff) do { pv_one<0>(o0, vb0 + (boff), pa0, pa1, pa2, pa3); pv_one<1>(o1, vb0 + (boff), pa0, pa1, pa2, pa3); } while (0)
; #define RESC(a) do { if (__any((a) < 1.f)) { _Pragma("unroll") for (int r = 0; r < 16; ++r) { o0[r] *= (a); o1[r] *= (a); } } } while (0)
; template <int DQK, bool FIXM> ...
;     ...
;     __syncthreads();
;     SBAR(); qkt<DQK>(pB0, pB1, lds + bK, qr, r32, hi, negm);
;     finishSM(pA0, pA1, alA, l_reg, pa0, pa1, pa2, pa3); SBAR();
;     if constexpr (FIXM) pv_psm<true>(o0, o1, vb0 + bV, pa0, pa1, pa2, pa3, pB0, pB1, m_reg, negm, alB); else { PVO(bV); partialSM<false>(pB0, pB1, m_reg, negm, alB); }
;     if (!FIXM) RESC(alB);
;     finishSM(pB0, pB1, alB, l_reg, pa0, pa1, pa2, pa3); SBAR();
;     PVO(bK);
.Lmla_exit_0:
	s_mov_b32 s11, 0
	s_mov_b32 s37, 0
	s_mov_b32 s13, 20480
	s_mov_b32 s10, 40960
	s_branch .Lmla_exit

; #define SBAR() __builtin_amdgcn_sched_barrier(0)
; #define PVO(boff) do { pv_one<0>(o0, vb0 + (boff), pa0, pa1, pa2, pa3); pv_one<1>(o1, vb0 + (boff), pa0, pa1, pa2, pa3); } while (0)
; #define RESC(a) do { if (__any((a) < 1.f)) { _Pragma("unroll") for (int r = 0; r < 16; ++r) { o0[r] *= (a); o1[r] *= (a); } } } while (0)
; template <int DQK, bool FIXM> ...
;     ...
;     __syncthreads();
;     SBAR(); qkt<DQK>(pB0, pB1, lds + bK, qr, r32, hi, negm);
;     finishSM(pA0, pA1, alA, l_reg, pa0, pa1, pa2, pa3); SBAR();
;     if constexpr (FIXM) pv_psm<true>(o0, o1, vb0 + bV, pa0, pa1, pa2, pa3, pB0, pB1, m_reg, negm, alB); else { PVO(bV); partialSM<false>(pB0, pB1, m_reg, negm, alB); }
;     if (!FIXM) RESC(alB);
;     finishSM(pB0, pB1, alB, l_reg, pa0, pa1, pa2, pa3); SBAR();
;     PVO(bK);
.Lmla_exit_1:
	s_mov_b32 s11, 40960
	s_mov_b32 s37, 40960
	s_mov_b32 s13, 0
	s_mov_b32 s10, 20480
	s_branch .Lmla_exit

; #define SBAR() __builtin_amdgcn_sched_barrier(0)
; #define PVO(boff) do { pv_one<0>(o0, vb0 + (boff), pa0, pa1, pa2, pa3); pv_one<1>(o1, vb0 + (boff), pa0, pa1, pa2, pa3); } while (0)
; #define RESC(a) do { if (__any((a) < 1.f)) { _Pragma("unroll") for (int r = 0; r < 16; ++r) { o0[r] *= (a); o1[r] *= (a); } } } while (0)
; template <int DQK, bool FIXM> ...
;     ...
;     __syncthreads();
;     SBAR(); qkt<DQK>(pB0, pB1, lds + bK, qr, r32, hi, negm);
;     finishSM(pA0, pA1, alA, l_reg, pa0, pa1, pa2, pa3); SBAR();
;     if constexpr (FIXM) pv_psm<true>(o0, o1, vb0 + bV, pa0, pa1, pa2, pa3, pB0, pB1, m_reg, negm, alB); else { PVO(bV); partialSM<false>(pB0, pB1, m_reg, negm, alB); }
;     if (!FIXM) RESC(alB);
;     finishSM(pB0, pB1, alB, l_reg, pa0, pa1, pa2, pa3); SBAR();
;     PVO(bK);
.Lmla_exit_2:
	s_mov_b32 s11, 20480
	s_mov_b32 s37, 20480
	s_mov_b32 s13, 40960
	s_mov_b32 s10, 0
	s_branch .Lmla_exit
.Lmla_exit:
	v_sub_u32_e32 v209, v209, v201
	v_sub_u32_e32 v210, v210, v201
	v_sub_u32_e32 v211, v211, v201
	v_sub_u32_e32 v212, v212, v201
	v_sub_u32_e32 v219, v219, v217
	v_sub_u32_e32 v220, v220, v217
	v_add_u32_e32 v17, s11, v213
	v_mov_b64_e32 v[66:67], v[82:83]
	v_mov_b64_e32 v[68:69], v[84:85]
	v_mov_b64_e32 v[70:71], v[86:87]
	v_mov_b64_e32 v[72:73], v[88:89]
	v_mov_b64_e32 v[74:75], v[90:91]
	v_mov_b64_e32 v[76:77], v[92:93]
	v_mov_b64_e32 v[78:79], v[94:95]
	v_mov_b64_e32 v[80:81], v[96:97]
	s_branch .LBB0_544
